# conversion split retuned: 4096 more layer-0 items in top-k phase (L0_B 0x6000), 4096 more layer-1 items in top-k phase (L1_A 0x9800), plus counted-wait conversion loops
# speedup vs baseline: 1.0104x; 1.0102x over previous
;     __device__ __forceinline__ const float* x() const { return (const float*)ld(0); }
; __device__ __forceinline__ void convert_moe_items(const Ctx& a, int layer, LAS unsigned char* lds, int it0, int it1, int widx, int nw, int wave, int lane) {
;     ...
;     int it = it0 + widx;
;     if (it >= it1) return;
;     f32x4 va[8], vb[8]; CvtItem da = decode(it), db = da; bool hb = (it + nw < it1);
;     cvt_load(da, va, lane);
;     if (hb) { db = decode(it + nw); cvt_load(db, vb, lane); }
; PHASE_FN ph_win() { PH_PRO;
;     ...
;     { const int nu = S.total(), maxu = (nu + G - 1) / G, nfull = nu - (maxu - 1) * G;
;       if ((int)blockIdx.x >= nfull && nfull < G) convert_moe_items(a, 0, lds, L0_B, MOE_ITEMS, ((int)blockIdx.x - nfull) * NWAVES + wave, (G - nfull) * NWAVES, wave, lane);
.LBB0_348:
	s_waitcnt lgkmcnt(0)
	s_abs_i32 s0, s47
	v_cvt_f32_u32_e32 v2, s0
	s_sub_i32 s3, 0, s0
	s_add_i32 s1, s47, 0x287
	s_xor_b32 s2, s1, s47
	v_rcp_iflag_f32_e32 v2, v2
	s_abs_i32 s1, s1
	s_ashr_i32 s2, s2, 31
	v_mul_f32_e32 v2, 0x4f7ffffe, v2
	v_cvt_u32_f32_e32 v2, v2
	s_nop 0
	v_readfirstlane_b32 s4, v2
	s_mul_i32 s3, s3, s4
	s_mul_hi_u32 s3, s4, s3
	s_add_i32 s4, s4, s3
	s_mul_hi_u32 s3, s1, s4
	s_mul_i32 s4, s3, s0
	s_sub_i32 s1, s1, s4
	s_add_i32 s5, s3, 1
	s_sub_i32 s4, s1, s0
	s_cmp_ge_u32 s1, s0
	s_cselect_b32 s3, s5, s3
	s_cselect_b32 s1, s4, s1
	s_add_i32 s4, s3, 1
	s_cmp_ge_u32 s1, s0
	s_cselect_b32 s0, s4, s3
	s_xor_b32 s0, s0, s2
	s_sub_i32 s28, s0, s2
	s_add_i32 s0, s28, -1
	s_mul_i32 s0, s0, s47
	s_sub_i32 s29, 0x288, s0
	s_cmp_lt_i32 s96, s29
	s_cselect_b64 s[2:3], -1, 0
	s_cmp_le_i32 s47, s29
	s_cselect_b64 s[0:1], -1, 0
	s_or_b64 s[4:5], s[2:3], s[0:1]
	s_mov_b64 s[2:3], -1
	s_and_b64 vcc, exec, s[4:5]
	s_cbranch_vccz .LBB0_423
	s_lshl_b32 s2, s96, 3
	s_andn2_b64 vcc, exec, s[0:1]
	s_add_i32 s30, s58, s2
	s_cbranch_vccnz .LBB0_354
	s_add_i32 s0, 0, 0x23f10
	v_mov_b32_e32 v2, s0
	s_add_i32 s0, 0, 0x23ee8
	v_mov_b32_e32 v4, s0
	s_add_i32 s0, 0, 0x23ef8
	s_waitcnt vmcnt(0)
	v_mov_b32_e32 v8, s0
	ds_read_b64 v[2:3], v2
	ds_read2_b64 v[4:7], v4 offset1:1
	ds_read_b64 v[8:9], v8
	s_lshl_b32 s31, s47, 3
	s_cmpk_gt_i32 s30, 0x5fff
	s_waitcnt lgkmcnt(2)
	v_readfirstlane_b32 s2, v3
	v_readfirstlane_b32 s3, v2
	s_waitcnt lgkmcnt(1)
	v_readfirstlane_b32 s33, v5
	v_readfirstlane_b32 s34, v4
	v_readfirstlane_b32 s35, v7
	v_readfirstlane_b32 s36, v6
	s_waitcnt lgkmcnt(0)
	v_readfirstlane_b32 s37, v9
	v_readfirstlane_b32 s38, v8
	s_cbranch_scc1 .LBB0_401
	s_add_u32 s0, s3, 0x2530000
	s_addc_u32 s1, s2, 0
	s_add_u32 s4, s3, 0x12530000
	s_addc_u32 s5, s2, 0
	s_add_i32 s41, s30, 0x6000
	s_mul_hi_i32 s2, s41, 0x2aaaaaab
	s_lshr_b32 s3, s2, 31
	s_ashr_i32 s2, s2, 9
	s_add_i32 s2, s2, s3
	s_mul_i32 s3, s2, 0xc00
	s_sub_i32 s13, s41, s3
	s_ashr_i32 s3, s2, 31
	s_lshl_b64 s[8:9], s[2:3], 21
	s_lshl_b32 s17, s2, 11
	s_cmpk_gt_i32 s13, 0x3ff
	s_cbranch_scc0 .LBB0_355
	s_cmpk_gt_u32 s13, 0x7ff
	s_cbranch_scc0 .LBB0_356
	s_add_i32 s16, s13, 0xfffff800
	s_lshl_b64 s[2:3], s[8:9], 2
	s_add_u32 s2, s38, s2
	s_addc_u32 s3, s37, s3
	s_mov_b64 s[6:7], 0
	s_branch .LBB0_357

;     __device__ __forceinline__ const float* x() const { return (const float*)ld(0); }
; __device__ __forceinline__ void convert_moe_items(const Ctx& a, int layer, LAS unsigned char* lds, int it0, int it1, int widx, int nw, int wave, int lane) {
;     ...
;     int it = it0 + widx;
;     if (it >= it1) return;
;     f32x4 va[8], vb[8]; CvtItem da = decode(it), db = da; bool hb = (it + nw < it1);
;     cvt_load(da, va, lane);
;     if (hb) { db = decode(it + nw); cvt_load(db, vb, lane); }
; PHASE_FN ph_win() { PH_PRO;
;     ...
;     { const int nu = S.total(), maxu = (nu + G - 1) / G, nfull = nu - (maxu - 1) * G;
;       if ((int)blockIdx.x >= nfull && nfull < G) convert_moe_items(a, 0, lds, L0_B, MOE_ITEMS, ((int)blockIdx.x - nfull) * NWAVES + wave, (G - nfull) * NWAVES, wave, lane);
.LBB0_423:
	s_andn2_b64 vcc, exec, s[2:3]
	s_cbranch_vccnz .LBB0_471
	s_sub_i32 s0, s96, s29
	s_lshl_b32 s2, s0, 3
	s_add_i32 s0, 0, 0x23f10
	v_mov_b32_e32 v2, s0
	s_waitcnt vmcnt(0)
	ds_read_b64 v[6:7], v2
	s_add_i32 s0, 0, 0x23ee8
	v_mov_b32_e32 v2, s0
	s_add_i32 s0, 0, 0x23ef8
	ds_read2_b64 v[2:5], v2 offset1:1
	s_waitcnt lgkmcnt(1)
	v_readfirstlane_b32 s4, v6
	v_mov_b32_e32 v6, s0
	v_readfirstlane_b32 s3, v7
	ds_read_b64 v[6:7], v6
	s_add_i32 s2, s2, s58
	s_waitcnt lgkmcnt(1)
	v_readfirstlane_b32 s30, v3
	v_readfirstlane_b32 s31, v2
	v_readfirstlane_b32 s33, v5
	v_readfirstlane_b32 s34, v4
	s_waitcnt lgkmcnt(0)
	v_readfirstlane_b32 s35, v7
	s_cmpk_gt_u32 s2, 0x5fff
	v_readfirstlane_b32 s36, v6
	s_cbranch_scc1 .LBB0_471
	s_add_u32 s0, s4, 0x2530000
	s_addc_u32 s1, s3, 0
	s_add_u32 s4, s4, 0x12530000
	s_addc_u32 s5, s3, 0
	s_add_i32 s39, s2, 0x6000
	s_and_b32 s2, s39, 0xffff
	s_mul_i32 s2, s2, 0xaaab
	s_lshr_b32 s2, s2, 27
	s_mul_i32 s3, s2, 0xc00
	s_sub_i32 s3, s39, s3
	s_and_b32 s10, s3, 0xffff
	s_lshl_b32 s16, s2, 21
	s_lshl_b32 s11, s2, 11
	s_cmpk_gt_u32 s10, 0x3ff
	s_cbranch_scc0 .LBB0_430
	s_cmpk_gt_u32 s10, 0x7ff
	s_cbranch_scc0 .LBB0_436
	s_add_i32 s13, s10, 0xfffff800
	s_lshl_b32 s2, s16, 2
	s_add_u32 s2, s36, s2
	s_addc_u32 s3, s35, 0
	s_mov_b32 s27, 1
	s_cbranch_execz .LBB0_437
	s_movk_i32 s12, 0x800
	s_movk_i32 s37, 0x400
	s_mov_b32 s27, 0
	s_mov_b32 s38, s11
	s_mov_b64 s[6:7], s[4:5]
	s_cbranch_execz .LBB0_431
	s_branch .LBB0_432

;     __device__ __forceinline__ const float* x() const { return (const float*)ld(0); }
;     __device__ __forceinline__ unsigned char* ws() const { return (unsigned char*)ld(26); }
; PHASE_FN ph_wout(unsigned* dep, const XcdBarrier& bar) { PH_PRO;
;     unsigned char* ws = a.ws();
;     const int GH = (G >= 2) ? G / 2 : G;
;     if ((int)blockIdx.x < GH) {
;         if (dep) dep_wait(dep, bar);
;         const pg8::Geo g = pg8::geo_rowmajor(ws + WS_CAT, DM, ws + WS_WOUT, DM, DM);
;         pg8::StaticOrder S; S.init(SEQ, DM, GH, (int)blockIdx.x);
;         pg8::EpiResid<true> E{a.x(), (_Float16*)(ws + WS_X), (const float*)(ws + WS_MODL) + 2 * DM};
;         pg8::gemm_phase<pg8::EpiResid<true>, pg8::StaticOrder, true, true>(lds, g, S, E);
;         if (GH == G) convert_moe_items(a, 1, lds, 0, L1_A, gw, NGW, wave, lane);
;     } else convert_moe_items(a, 1, lds, 0, L1_A, ((int)blockIdx.x - GH) * NWAVES + wave, (G - GH) * NWAVES, wave, lane);
.LBB0_650:
	s_cmp_lt_i32 s94, 5
	s_cselect_b64 s[2:3], -1, 0
	s_and_b64 s[8:9], s[2:3], s[0:1]
	s_andn2_b64 vcc, exec, s[8:9]
	s_cbranch_vccnz .LBB0_791
	v_readlane_b32 s0, v248, 0
	v_readlane_b32 s1, v248, 1
	s_load_dword s43, s[0:1], 0xe0
	s_add_i32 s0, 0, 0x23f10
	v_mov_b32_e32 v1, s0
	v_readfirstlane_b32 s0, v0
	s_lshr_b32 s44, s0, 6
	s_waitcnt lgkmcnt(0)
	s_lshl_b32 s42, s43, 3
	s_waitcnt vmcnt(0)
	ds_read_b64 v[2:3], v1
	s_cmp_gt_i32 s43, 1
	s_cselect_b64 s[0:1], -1, 0
	v_cndmask_b32_e64 v1, 0, 1, s[0:1]
	s_waitcnt lgkmcnt(0)
	v_readfirstlane_b32 s30, v3
	v_readfirstlane_b32 s0, v1
	s_lshr_b32 s45, s43, s0
	v_readfirstlane_b32 s31, v2
	s_cmp_ge_i32 s96, s45
	s_mov_b64 s[0:1], -1
	s_cbranch_scc0 .LBB0_699
	s_sub_i32 s0, s96, s45
	s_lshl_b32 s0, s0, 3
	s_add_i32 s41, s0, s44
	s_add_i32 s0, 0, 0x23ee8
	v_mov_b32_e32 v1, s0
	s_add_i32 s0, 0, 0x23ef8
	ds_read2_b64 v[4:7], v1 offset1:1
	v_mov_b32_e32 v1, s0
	v_readfirstlane_b32 s2, v3
	v_readfirstlane_b32 s3, v2
	ds_read_b64 v[2:3], v1
	s_waitcnt lgkmcnt(1)
	v_readfirstlane_b32 s33, v5
	v_readfirstlane_b32 s34, v4
	v_readfirstlane_b32 s35, v7
	v_readfirstlane_b32 s36, v6
	s_waitcnt lgkmcnt(0)
	v_readfirstlane_b32 s37, v3
	s_cmpk_gt_u32 s41, 0x97ff
	v_readfirstlane_b32 s38, v2
	s_cbranch_scc1 .LBB0_698
	s_add_u32 s0, s3, 0xa530000
	s_addc_u32 s1, s2, 0
	s_add_u32 s4, s3, 0x16530000
	s_addc_u32 s5, s2, 0
	s_and_b32 s2, s41, 0xffff
	s_mul_i32 s2, s2, 0xaaab
	s_lshr_b32 s2, s2, 27
	s_mul_i32 s3, s2, 0xc00
	s_sub_i32 s3, s41, s3
	s_lshl_b32 s18, s2, 21
	s_and_b32 s14, s3, 0xffff
	s_add_i32 s18, s18, 0x2000000
	s_lshl_b32 s15, s2, 11
	s_cmpk_gt_u32 s14, 0x3ff
	s_cbranch_scc0 .LBB0_657
	s_cmpk_gt_u32 s14, 0x7ff
	s_cbranch_scc0 .LBB0_663
	s_add_i32 s17, s14, 0xfffff800
	s_lshl_b32 s2, s18, 2
	s_add_u32 s2, s38, s2
	s_addc_u32 s3, s37, 0
	s_mov_b32 s29, 1
	s_cbranch_execz .LBB0_664
	s_movk_i32 s16, 0x800
	s_movk_i32 s39, 0x400
	s_mov_b32 s29, 0
	s_mov_b32 s40, s15
	s_mov_b64 s[10:11], s[4:5]
	s_cbranch_execz .LBB0_658
	s_branch .LBB0_659

; __device__ __forceinline__ void cvt_load(const CvtItem& d, f32x4 (&v)[8], int lane) {
;     const float* p = d.src + (size_t)(d.k0 + (lane >> 3)) * d.N + d.n0 + (lane & 7) * 4;
; #pragma unroll
;     for (int q = 0; q < 8; ++q) v[q] = __builtin_nontemporal_load((const f32x4*)(p + (size_t)(8 * q) * d.N));
; }
; __device__ __forceinline__ void convert_moe_items(const Ctx& a, int layer, LAS unsigned char* lds, int it0, int it1, int widx, int nw, int wave, int lane) {
;     ...
;     int it = it0 + widx;
;     if (it >= it1) return;
;     f32x4 va[8], vb[8]; CvtItem da = decode(it), db = da; bool hb = (it + nw < it1);
;     cvt_load(da, va, lane);
;     if (hb) { db = decode(it + nw); cvt_load(db, vb, lane); }
.LBB0_659:
	s_lshr_b32 s14, s16, 5
	s_ff1_i32_b32 s12, s14
	s_lshr_b32 s12, s17, s12
	s_and_b32 s12, s12, 0xffff
	s_lshl_b32 s12, s12, 6
	v_lshrrev_b32_e32 v1, 3, v214
	s_sub_i32 s13, s43, s45
	s_add_i32 s14, s14, -1
	v_or_b32_e32 v2, s12, v1
	s_lshl_b32 s15, s13, 3
	s_and_b32 s14, s14, s17
	s_mov_b32 s17, 0
	v_mul_hi_u32_u24_e32 v3, s16, v2
	v_mul_u32_u24_e32 v2, s16, v2
	v_lshlrev_b32_e32 v4, 2, v0
	s_lshl_b32 s14, s14, 5
	s_add_i32 s20, s41, s15
	v_lshl_add_u64 v[2:3], v[2:3], 2, s[2:3]
	s_mov_b32 s15, s17
	v_and_b32_e32 v4, 28, v4
	s_cmp_lt_i32 s20, 0x9800
	v_lshl_add_u64 v[2:3], s[14:15], 2, v[2:3]
	v_mov_b32_e32 v67, 0
	v_lshlrev_b32_e32 v66, 2, v4
	s_cselect_b64 s[18:19], -1, 0
	s_lshl_b64 s[22:23], s[16:17], 5
	v_lshl_add_u64 v[10:11], v[2:3], 0, v[66:67]
	v_lshl_add_u64 v[12:13], v[10:11], 0, s[22:23]
	v_lshl_add_u64 v[18:19], v[12:13], 0, s[22:23]
	v_lshl_add_u64 v[20:21], v[18:19], 0, s[22:23]
	v_lshl_add_u64 v[26:27], v[20:21], 0, s[22:23]
	v_lshl_add_u64 v[28:29], v[26:27], 0, s[22:23]
	v_lshl_add_u64 v[34:35], v[28:29], 0, s[22:23]
	global_load_dwordx4 v[2:5], v[10:11], off nt
	global_load_dwordx4 v[6:9], v[12:13], off nt
	s_nop 0
	global_load_dwordx4 v[10:13], v[18:19], off nt
	global_load_dwordx4 v[14:17], v[20:21], off nt
	s_nop 0
	global_load_dwordx4 v[18:21], v[26:27], off nt
	global_load_dwordx4 v[22:25], v[28:29], off nt
	v_lshl_add_u64 v[36:37], v[34:35], 0, s[22:23]
	global_load_dwordx4 v[26:29], v[34:35], off nt
	global_load_dwordx4 v[30:33], v[36:37], off nt
	s_cmp_gt_i32 s20, 0x97ff
	s_mov_b64 s[16:17], s[10:11]
	s_mov_b32 s47, s39
	s_mov_b32 s48, s40
	s_mov_b32 s46, s29
	s_mov_b32 s22, s12
	s_mov_b32 s24, s14
	s_cbranch_scc1 .LBB0_674
	s_mul_hi_i32 s2, s20, 0x2aaaaaab
	s_lshr_b32 s3, s2, 31
	s_ashr_i32 s2, s2, 9
	s_add_i32 s2, s2, s3
	s_mul_i32 s3, s2, 0xc00
	s_sub_i32 s21, s20, s3
	s_ashr_i32 s3, s2, 31
	s_lshl_b64 s[16:17], s[2:3], 21
	s_add_u32 s22, s16, 0x2000000
	s_addc_u32 s23, s17, 0
	s_lshl_b32 s26, s2, 11
	s_cmpk_gt_i32 s21, 0x3ff
	s_cbranch_scc0 .LBB0_665
	s_cmpk_gt_u32 s21, 0x7ff
	s_cbranch_scc0 .LBB0_666
	s_add_i32 s15, s21, 0xfffff800
	s_lshl_b64 s[2:3], s[22:23], 2
	s_add_u32 s2, s38, s2
	s_addc_u32 s3, s37, s3
	s_mov_b64 s[16:17], 0
	s_branch .LBB0_667

; #define LAS __attribute__((address_space(3)))
; __device__ __forceinline__ unsigned pk2(float lo, float hi) { return f2bf(lo) | (f2bf(hi) << 16); }
;     __device__ __forceinline__ const float* x() const { return (const float*)ld(0); }
;     __device__ __forceinline__ const float* c() const { return (const float*)ld(1); }
; template <bool NT = true> __device__ __forceinline__ void cvt_store(const CvtItem& d, const f32x4 (&v)[8], LAS float* scr, int lane) {
;     const int rr = lane >> 3, c4 = (lane & 7) * 4;
; #pragma unroll
;     for (int q = 0; q < 8; ++q) { LAS float* t = scr + (8 * q + rr) * 33 + c4; t[0] = v[q].x; t[1] = v[q].y; t[2] = v[q].z; t[3] = v[q].w; }
;     asm volatile("s_waitcnt lgkmcnt(0)" ::: "memory");
;     const int c = lane & 7;
; #pragma unroll
;     for (int j = 0; j < 4; ++j) { const int n = (lane >> 3) + 8 * j; const LAS float* s = scr + (8 * c) * 33 + n;
;         u32x4 o; o.x = pk2(s[0 * 33], s[1 * 33]); o.y = pk2(s[2 * 33], s[3 * 33]); o.z = pk2(s[4 * 33], s[5 * 33]); o.w = pk2(s[6 * 33], s[7 * 33]);
;         const int ng = d.n0 + n, drow = d.row_off + (d.ilv ? ((ng >> 7) * 256 + (ng & 127)) : ng);
;         if (NT) __builtin_nontemporal_store(o, (u32x4*)(d.dst + (size_t)drow * d.K + d.k0 + 8 * c)); else *(u32x4*)(d.dst + (size_t)drow * d.K + d.k0 + 8 * c) = o; }
;     asm volatile("s_waitcnt lgkmcnt(0)" ::: "memory");
; __device__ __forceinline__ void convert_moe_items(const Ctx& a, int layer, LAS unsigned char* lds, int it0, int it1, int widx, int nw, int wave, int lane) {
;     ...
;     for (;;) {
;         cvt_store(da, va, scr, lane);
;         it += 2 * nw; const bool ha = (it < it1);
;         if (ha) { da = decode(it); cvt_load(da, va, lane); }
;         if (!hb) break;
.Lcvt_p4c_t:
	v_add_u32_e32 v79, 0x420, v74
	v_add_u32_e32 v80, 0x428, v74
	v_add_u32_e32 v81, 0x840, v74
	v_add_u32_e32 v82, 0x848, v74
	v_add_u32_e32 v83, 0xc60, v74
	v_add_u32_e32 v84, 0xc68, v74
	v_add_u32_e32 v85, 0x1080, v74
	v_add_u32_e32 v86, 0x1088, v74
	v_add_u32_e32 v87, 0x14a0, v74
	v_add_u32_e32 v88, 0x14a8, v74
	v_add_u32_e32 v89, 0x18c0, v74
	v_add_u32_e32 v90, 0x18c8, v74
	v_add_u32_e32 v91, 0x1ce0, v74
	v_add_u32_e32 v92, 0x1ce8, v74
	s_waitcnt vmcnt(15)
	ds_write2_b32 v74, v2, v3 offset1:1
	ds_write2_b32 v74, v4, v5 offset0:2 offset1:3
	s_waitcnt vmcnt(14)
	ds_write2_b32 v79, v6, v7 offset1:1
	ds_write2_b32 v80, v8, v9 offset1:1
	s_waitcnt vmcnt(13)
	ds_write2_b32 v81, v10, v11 offset1:1
	ds_write2_b32 v82, v12, v13 offset1:1
	s_waitcnt vmcnt(12)
	ds_write2_b32 v83, v14, v15 offset1:1
	ds_write2_b32 v84, v16, v17 offset1:1
	s_waitcnt vmcnt(11)
	ds_write2_b32 v85, v18, v19 offset1:1
	ds_write2_b32 v86, v20, v21 offset1:1
	s_waitcnt vmcnt(10)
	ds_write2_b32 v87, v22, v23 offset1:1
	ds_write2_b32 v88, v24, v25 offset1:1
	s_waitcnt vmcnt(9)
	ds_write2_b32 v89, v26, v27 offset1:1
	ds_write2_b32 v90, v28, v29 offset1:1
	s_waitcnt vmcnt(8)
	ds_write2_b32 v91, v30, v31 offset1:1
	ds_write2_b32 v92, v32, v33 offset1:1
	s_waitcnt lgkmcnt(0)
	ds_read2_b32 v[98:99], v73 offset1:8
	ds_read2_b32 v[100:101], v73 offset0:33 offset1:41
	ds_read2_b32 v[102:103], v73 offset0:66 offset1:74
	ds_read2_b32 v[104:105], v73 offset0:99 offset1:107
	ds_read2_b32 v[106:107], v73 offset0:132 offset1:140
	s_waitcnt lgkmcnt(4)
	v_bfe_u32 v67, v98, 16, 1
	v_add3_u32 v67, v98, v67, s51
	s_waitcnt lgkmcnt(3)
	v_bfe_u32 v93, v100, 16, 1
	v_lshrrev_b32_e32 v67, 16, v67
	v_add3_u32 v93, v100, v93, s51
	ds_read2_b32 v[108:109], v73 offset0:165 offset1:173
	v_and_or_b32 v94, v93, s52, v67
	s_waitcnt lgkmcnt(3)
	v_bfe_u32 v67, v102, 16, 1
	v_add3_u32 v67, v102, v67, s51
	s_waitcnt lgkmcnt(2)
	v_bfe_u32 v93, v104, 16, 1
	ds_read2_b32 v[110:111], v73 offset0:198 offset1:206
	v_lshrrev_b32_e32 v67, 16, v67
	v_add3_u32 v93, v104, v93, s51
	ds_read2_b32 v[112:113], v73 offset0:231 offset1:239
	v_and_or_b32 v95, v93, s52, v67
	s_waitcnt lgkmcnt(3)
	v_bfe_u32 v67, v106, 16, 1
	v_add3_u32 v67, v106, v67, s51
	s_waitcnt lgkmcnt(2)
	v_bfe_u32 v93, v108, 16, 1
	v_lshrrev_b32_e32 v67, 16, v67
	v_add3_u32 v93, v108, v93, s51
	v_and_or_b32 v96, v93, s52, v67
	s_waitcnt lgkmcnt(1)
	v_bfe_u32 v67, v110, 16, 1
	v_add3_u32 v67, v110, v67, s51
	s_waitcnt lgkmcnt(0)
	v_bfe_u32 v93, v112, 16, 1
	s_cmp_eq_u32 s29, 0
	v_lshrrev_b32_e32 v67, 16, v67
	v_add3_u32 v93, v112, v93, s51
	s_cselect_b64 vcc, -1, 0
	s_lshl_b32 s2, s14, 1
	v_and_or_b32 v97, v93, s52, v67
	s_and_b32 s15, s2, 0xffffff00
	v_bitop3_b32 v93, s14, v75, v1 bitop3:0xc8
	v_or_b32_e32 v67, s14, v1
	v_or_b32_e32 v93, s15, v93
	v_cndmask_b32_e32 v67, v93, v67, vcc
	v_add_u32_e32 v67, s40, v67
	v_mad_u64_u32 v[114:115], s[2:3], v67, s39, 0
	v_ashrrev_i32_e32 v93, 31, v67
	v_mov_b32_e32 v98, v115
	v_mad_u64_u32 v[116:117], s[2:3], v93, s39, v[98:99]
	v_mov_b32_e32 v115, v116
	s_ashr_i32 s13, s12, 31
	v_lshl_add_u64 v[114:115], v[114:115], 1, s[10:11]
	s_lshl_b64 s[2:3], s[12:13], 1
	v_bfe_u32 v67, v99, 16, 1
	v_lshl_add_u64 v[114:115], v[114:115], 0, s[2:3]
	v_add3_u32 v67, v99, v67, s51
	v_bfe_u32 v93, v101, 16, 1
	v_lshl_add_u64 v[114:115], v[114:115], 0, v[68:69]
	v_lshrrev_b32_e32 v67, 16, v67
	v_add3_u32 v93, v101, v93, s51
	global_store_dwordx4 v[114:115], v[94:97], off nt
	s_add_i32 s54, s41, s49
	s_cmp_gt_i32 s54, 0x97ff
	v_and_or_b32 v94, v93, s52, v67
	v_bfe_u32 v67, v103, 16, 1
	v_add3_u32 v67, v103, v67, s51
	v_bfe_u32 v93, v105, 16, 1
	v_lshrrev_b32_e32 v67, 16, v67
	v_add3_u32 v93, v105, v93, s51
	v_and_or_b32 v95, v93, s52, v67
	v_bfe_u32 v67, v107, 16, 1
	v_add3_u32 v67, v107, v67, s51
	v_bfe_u32 v93, v109, 16, 1
	v_lshrrev_b32_e32 v67, 16, v67
	v_add3_u32 v93, v109, v93, s51
	v_and_or_b32 v96, v93, s52, v67
	v_bfe_u32 v67, v111, 16, 1
	v_add3_u32 v67, v111, v67, s51
	v_bfe_u32 v93, v113, 16, 1
	v_lshrrev_b32_e32 v67, 16, v67
	v_add3_u32 v93, v113, v93, s51
	v_and_or_b32 v97, v93, s52, v67
	v_bitop3_b32 v93, s14, v76, v70 bitop3:0xc8
	v_or_b32_e32 v67, s14, v70
	v_or_b32_e32 v93, s15, v93
	v_cndmask_b32_e32 v67, v93, v67, vcc
	v_add_u32_e32 v67, s40, v67
	v_mad_u64_u32 v[98:99], s[26:27], v67, s39, 0
	v_ashrrev_i32_e32 v93, 31, v67
	v_mov_b32_e32 v100, v99
	v_mad_u64_u32 v[100:101], s[26:27], v93, s39, v[100:101]
	v_mov_b32_e32 v99, v100
	v_lshl_add_u64 v[98:99], v[98:99], 1, s[10:11]
	v_lshl_add_u64 v[98:99], v[98:99], 0, s[2:3]
	ds_read2_b32 v[100:101], v73 offset0:16 offset1:24
	v_lshl_add_u64 v[98:99], v[98:99], 0, v[68:69]
	global_store_dwordx4 v[98:99], v[94:97], off nt
	ds_read2_b32 v[98:99], v73 offset0:49 offset1:57
	ds_read2_b32 v[102:103], v73 offset0:82 offset1:90
	ds_read2_b32 v[104:105], v73 offset0:115 offset1:123
	s_waitcnt lgkmcnt(3)
; #define LAS __attribute__((address_space(3)))
; __device__ __forceinline__ unsigned pk2(float lo, float hi) { return f2bf(lo) | (f2bf(hi) << 16); }
;     __device__ __forceinline__ const float* x() const { return (const float*)ld(0); }
;     __device__ __forceinline__ const float* c() const { return (const float*)ld(1); }
; template <bool NT = true> __device__ __forceinline__ void cvt_store(const CvtItem& d, const f32x4 (&v)[8], LAS float* scr, int lane) {
;     const int rr = lane >> 3, c4 = (lane & 7) * 4;
; #pragma unroll
;     for (int q = 0; q < 8; ++q) { LAS float* t = scr + (8 * q + rr) * 33 + c4; t[0] = v[q].x; t[1] = v[q].y; t[2] = v[q].z; t[3] = v[q].w; }
;     asm volatile("s_waitcnt lgkmcnt(0)" ::: "memory");
;     const int c = lane & 7;
; #pragma unroll
;     for (int j = 0; j < 4; ++j) { const int n = (lane >> 3) + 8 * j; const LAS float* s = scr + (8 * c) * 33 + n;
;         u32x4 o; o.x = pk2(s[0 * 33], s[1 * 33]); o.y = pk2(s[2 * 33], s[3 * 33]); o.z = pk2(s[4 * 33], s[5 * 33]); o.w = pk2(s[6 * 33], s[7 * 33]);
;         const int ng = d.n0 + n, drow = d.row_off + (d.ilv ? ((ng >> 7) * 256 + (ng & 127)) : ng);
;         if (NT) __builtin_nontemporal_store(o, (u32x4*)(d.dst + (size_t)drow * d.K + d.k0 + 8 * c)); else *(u32x4*)(d.dst + (size_t)drow * d.K + d.k0 + 8 * c) = o; }
;     asm volatile("s_waitcnt lgkmcnt(0)" ::: "memory");
; __device__ __forceinline__ void convert_moe_items(const Ctx& a, int layer, LAS unsigned char* lds, int it0, int it1, int widx, int nw, int wave, int lane) {
;     ...
;     auto decode = [&](int it) { CvtItem d; const int e = it / PER_E; int r = it % PER_E; const size_t eo = ((size_t)layer * NE + e) * (size_t)DM * FE;
;         if (r < I_G)          { d.src = wg + eo; d.dst = WGU; d.N = FE; d.K = DM; d.row_off = e * 2048; d.ilv = 1; }
;         else if (r < 2 * I_G) { r -= I_G; d.src = wu + eo; d.dst = WGU; d.N = FE; d.K = DM; d.row_off = e * 2048 + 128; d.ilv = 1; }
;         else                  { r -= 2 * I_G; d.src = wd + eo; d.dst = WD; d.N = DM; d.K = FE; d.row_off = e * 2048; d.ilv = 0; }
;         const int nblk = d.N / 32; d.k0 = 64 * (r / nblk); d.n0 = 32 * (r % nblk); return d; };
	v_bfe_u32 v67, v100, 16, 1
	v_add3_u32 v67, v100, v67, s51
	s_waitcnt lgkmcnt(2)
	v_bfe_u32 v93, v98, 16, 1
	ds_read2_b32 v[106:107], v73 offset0:148 offset1:156
	v_lshrrev_b32_e32 v67, 16, v67
	v_add3_u32 v93, v98, v93, s51
	ds_read2_b32 v[108:109], v73 offset0:181 offset1:189
	v_and_or_b32 v94, v93, s52, v67
	s_waitcnt lgkmcnt(3)
	v_bfe_u32 v67, v102, 16, 1
	v_add3_u32 v67, v102, v67, s51
	s_waitcnt lgkmcnt(2)
	v_bfe_u32 v93, v104, 16, 1
	ds_read2_b32 v[110:111], v73 offset0:214 offset1:222
	v_lshrrev_b32_e32 v67, 16, v67
	v_add3_u32 v93, v104, v93, s51
	ds_read2_b32 v[112:113], v73 offset0:247 offset1:255
	v_and_or_b32 v95, v93, s52, v67
	s_waitcnt lgkmcnt(3)
	v_bfe_u32 v67, v106, 16, 1
	v_add3_u32 v67, v106, v67, s51
	s_waitcnt lgkmcnt(2)
	v_bfe_u32 v93, v108, 16, 1
	v_lshrrev_b32_e32 v67, 16, v67
	v_add3_u32 v93, v108, v93, s51
	v_and_or_b32 v96, v93, s52, v67
	s_waitcnt lgkmcnt(1)
	v_bfe_u32 v67, v110, 16, 1
	v_add3_u32 v67, v110, v67, s51
	s_waitcnt lgkmcnt(0)
	v_bfe_u32 v93, v112, 16, 1
	v_lshrrev_b32_e32 v67, 16, v67
	v_add3_u32 v93, v112, v93, s51
	v_and_or_b32 v97, v93, s52, v67
	v_bitop3_b32 v93, s14, v77, v71 bitop3:0xc8
	v_or_b32_e32 v67, s14, v71
	v_or_b32_e32 v93, s15, v93
	v_cndmask_b32_e32 v67, v93, v67, vcc
	v_add_u32_e32 v67, s40, v67
	v_mad_u64_u32 v[114:115], s[26:27], v67, s39, 0
	v_ashrrev_i32_e32 v93, 31, v67
	v_mov_b32_e32 v98, v115
	v_mad_u64_u32 v[116:117], s[26:27], v93, s39, v[98:99]
	v_mov_b32_e32 v115, v116
	v_lshl_add_u64 v[114:115], v[114:115], 1, s[10:11]
	v_bfe_u32 v67, v101, 16, 1
	v_lshl_add_u64 v[114:115], v[114:115], 0, s[2:3]
	v_add3_u32 v67, v101, v67, s51
	v_bfe_u32 v93, v99, 16, 1
	v_lshl_add_u64 v[114:115], v[114:115], 0, v[68:69]
	v_lshrrev_b32_e32 v67, 16, v67
	v_add3_u32 v93, v99, v93, s51
	global_store_dwordx4 v[114:115], v[94:97], off nt
	s_nop 1
	v_and_or_b32 v94, v93, s52, v67
	v_bfe_u32 v67, v103, 16, 1
	v_add3_u32 v67, v103, v67, s51
	v_bfe_u32 v93, v105, 16, 1
	v_lshrrev_b32_e32 v67, 16, v67
	v_add3_u32 v93, v105, v93, s51
	v_and_or_b32 v95, v93, s52, v67
	v_bfe_u32 v67, v107, 16, 1
	v_add3_u32 v67, v107, v67, s51
	v_bfe_u32 v93, v109, 16, 1
	v_lshrrev_b32_e32 v67, 16, v67
	v_add3_u32 v93, v109, v93, s51
	v_and_or_b32 v96, v93, s52, v67
	v_bfe_u32 v67, v111, 16, 1
	v_add3_u32 v67, v111, v67, s51
	v_bfe_u32 v93, v113, 16, 1
	v_lshrrev_b32_e32 v67, 16, v67
	v_add3_u32 v93, v113, v93, s51
	v_and_or_b32 v97, v93, s52, v67
	v_bitop3_b32 v93, s14, v78, v72 bitop3:0xc8
	v_or_b32_e32 v67, s14, v72
	v_or_b32_e32 v93, s15, v93
	v_cndmask_b32_e32 v67, v93, v67, vcc
	v_add_u32_e32 v67, s40, v67
	v_mad_u64_u32 v[98:99], s[26:27], v67, s39, 0
	v_ashrrev_i32_e32 v93, 31, v67
	v_mov_b32_e32 v100, v99
	v_mad_u64_u32 v[100:101], s[26:27], v93, s39, v[100:101]
	v_mov_b32_e32 v99, v100
	v_lshl_add_u64 v[98:99], v[98:99], 1, s[10:11]
	v_lshl_add_u64 v[98:99], v[98:99], 0, s[2:3]
	v_lshl_add_u64 v[98:99], v[98:99], 0, v[68:69]
	global_store_dwordx4 v[98:99], v[94:97], off nt
	s_waitcnt lgkmcnt(0)
	s_cselect_b64 s[26:27], -1, 0
	s_and_b64 vcc, exec, s[26:27]
	s_cbranch_vccnz .LBB0_687
	s_mul_hi_i32 s2, s54, 0x2aaaaaab
	s_lshr_b32 s3, s2, 31
	s_ashr_i32 s2, s2, 9
	s_add_i32 s28, s2, s3
	s_mul_i32 s2, s28, 0xfffff400
	s_ashr_i32 s29, s28, 31
	s_add_i32 s23, s54, s2
	s_lshl_b64 s[2:3], s[28:29], 21
	s_add_u32 s12, s2, 0x2000000
	s_addc_u32 s13, s3, 0
	s_lshl_b32 s55, s28, 11
	s_cmpk_gt_i32 s23, 0x3ff
	s_mov_b64 s[14:15], -1
	s_cbranch_scc0 .LBB0_684
	s_mul_i32 s2, s28, 0xc00
	s_sub_i32 s14, s54, s2
	s_cmpk_gt_u32 s23, 0x7ff
	s_mov_b64 s[10:11], -1
	s_cbranch_scc0 .LBB0_682
	s_add_i32 s25, s14, 0xfffff800
	s_lshl_b64 s[2:3], s[12:13], 2
	s_add_u32 s2, s38, s2
	s_addc_u32 s3, s37, s3
	s_mov_b64 s[10:11], 0

; #define LAS __attribute__((address_space(3)))
; __device__ __forceinline__ unsigned pk2(float lo, float hi) { return f2bf(lo) | (f2bf(hi) << 16); }
;     __device__ __forceinline__ const float* x() const { return (const float*)ld(0); }
;     __device__ __forceinline__ const float* c() const { return (const float*)ld(1); }
; template <bool NT = true> __device__ __forceinline__ void cvt_store(const CvtItem& d, const f32x4 (&v)[8], LAS float* scr, int lane) {
;     const int rr = lane >> 3, c4 = (lane & 7) * 4;
; #pragma unroll
;     for (int q = 0; q < 8; ++q) { LAS float* t = scr + (8 * q + rr) * 33 + c4; t[0] = v[q].x; t[1] = v[q].y; t[2] = v[q].z; t[3] = v[q].w; }
;     asm volatile("s_waitcnt lgkmcnt(0)" ::: "memory");
;     const int c = lane & 7;
; #pragma unroll
;     for (int j = 0; j < 4; ++j) { const int n = (lane >> 3) + 8 * j; const LAS float* s = scr + (8 * c) * 33 + n;
;         u32x4 o; o.x = pk2(s[0 * 33], s[1 * 33]); o.y = pk2(s[2 * 33], s[3 * 33]); o.z = pk2(s[4 * 33], s[5 * 33]); o.w = pk2(s[6 * 33], s[7 * 33]);
;         const int ng = d.n0 + n, drow = d.row_off + (d.ilv ? ((ng >> 7) * 256 + (ng & 127)) : ng);
;         if (NT) __builtin_nontemporal_store(o, (u32x4*)(d.dst + (size_t)drow * d.K + d.k0 + 8 * c)); else *(u32x4*)(d.dst + (size_t)drow * d.K + d.k0 + 8 * c) = o; }
;     asm volatile("s_waitcnt lgkmcnt(0)" ::: "memory");
; __device__ __forceinline__ void convert_moe_items(const Ctx& a, int layer, LAS unsigned char* lds, int it0, int it1, int widx, int nw, int wave, int lane) {
;     ...
;         cvt_store(db, vb, scr, lane);
;         hb = (it + nw < it1);
;         if (hb) { db = decode(it + nw); cvt_load(db, vb, lane); }
.Lcvt_p4c_m:
	s_waitcnt vmcnt(12)
	ds_write2_b32 v74, v34, v35 offset1:1
	ds_write2_b32 v74, v36, v37 offset0:2 offset1:3
	ds_write2_b32 v79, v38, v39 offset1:1
	ds_write2_b32 v80, v40, v41 offset1:1
	ds_write2_b32 v81, v42, v43 offset1:1
	ds_write2_b32 v82, v44, v45 offset1:1
	ds_write2_b32 v83, v46, v47 offset1:1
	ds_write2_b32 v84, v48, v49 offset1:1
	ds_write2_b32 v85, v50, v51 offset1:1
	ds_write2_b32 v86, v52, v53 offset1:1
	ds_write2_b32 v87, v54, v55 offset1:1
	ds_write2_b32 v88, v56, v57 offset1:1
	ds_write2_b32 v89, v58, v59 offset1:1
	ds_write2_b32 v90, v60, v61 offset1:1
	ds_write2_b32 v91, v62, v63 offset1:1
	ds_write2_b32 v92, v64, v65 offset1:1
	s_waitcnt lgkmcnt(0)
	ds_read2_b32 v[84:85], v73 offset1:8
	ds_read2_b32 v[86:87], v73 offset0:33 offset1:41
	ds_read2_b32 v[88:89], v73 offset0:66 offset1:74
	ds_read2_b32 v[90:91], v73 offset0:99 offset1:107
	ds_read2_b32 v[92:93], v73 offset0:132 offset1:140
	s_waitcnt lgkmcnt(4)
	v_bfe_u32 v67, v84, 16, 1
	v_add3_u32 v67, v84, v67, s51
	s_waitcnt lgkmcnt(3)
	v_bfe_u32 v79, v86, 16, 1
	v_lshrrev_b32_e32 v67, 16, v67
	v_add3_u32 v79, v86, v79, s51
	ds_read2_b32 v[94:95], v73 offset0:165 offset1:173
	v_and_or_b32 v80, v79, s52, v67
	s_waitcnt lgkmcnt(3)
	v_bfe_u32 v67, v88, 16, 1
	v_add3_u32 v67, v88, v67, s51
	s_waitcnt lgkmcnt(2)
	v_bfe_u32 v79, v90, 16, 1
	ds_read2_b32 v[96:97], v73 offset0:198 offset1:206
	v_lshrrev_b32_e32 v67, 16, v67
	v_add3_u32 v79, v90, v79, s51
	ds_read2_b32 v[98:99], v73 offset0:231 offset1:239
	v_and_or_b32 v81, v79, s52, v67
	s_waitcnt lgkmcnt(3)
	v_bfe_u32 v67, v92, 16, 1
	v_add3_u32 v67, v92, v67, s51
	s_waitcnt lgkmcnt(2)
	v_bfe_u32 v79, v94, 16, 1
	v_lshrrev_b32_e32 v67, 16, v67
	v_add3_u32 v79, v94, v79, s51
	v_and_or_b32 v82, v79, s52, v67
	s_waitcnt lgkmcnt(1)
	v_bfe_u32 v67, v96, 16, 1
	v_add3_u32 v67, v96, v67, s51
	s_waitcnt lgkmcnt(0)
	v_bfe_u32 v79, v98, 16, 1
	v_lshrrev_b32_e32 v67, 16, v67
	v_add3_u32 v79, v98, v79, s51
	v_and_or_b32 v83, v79, s52, v67
	v_add_u32_e32 v67, s24, v1
	s_cmp_eq_u32 s46, 0
	v_lshlrev_b32_e32 v79, 1, v67
	v_and_b32_e32 v84, 0x7f, v67
	v_and_or_b32 v79, v79, s53, v84
	s_cselect_b64 vcc, -1, 0
	v_cndmask_b32_e32 v67, v79, v67, vcc
	v_add_u32_e32 v67, s48, v67
	v_mad_u64_u32 v[100:101], s[2:3], v67, s47, 0
	v_ashrrev_i32_e32 v79, 31, v67
	v_mov_b32_e32 v84, v101
	v_mad_u64_u32 v[102:103], s[2:3], v79, s47, v[84:85]
	v_mov_b32_e32 v101, v102
	s_ashr_i32 s23, s22, 31
	v_lshl_add_u64 v[100:101], v[100:101], 1, s[16:17]
	s_lshl_b64 s[2:3], s[22:23], 1
	v_bfe_u32 v67, v85, 16, 1
	v_lshl_add_u64 v[100:101], v[100:101], 0, s[2:3]
	v_add3_u32 v67, v85, v67, s51
	v_bfe_u32 v79, v87, 16, 1
	v_lshl_add_u64 v[100:101], v[100:101], 0, v[68:69]
	v_lshrrev_b32_e32 v67, 16, v67
	v_add3_u32 v79, v87, v79, s51
	global_store_dwordx4 v[100:101], v[80:83], off nt
	s_nop 1
	v_and_or_b32 v80, v79, s52, v67
	v_bfe_u32 v67, v89, 16, 1
	v_add3_u32 v67, v89, v67, s51
	v_bfe_u32 v79, v91, 16, 1
	v_lshrrev_b32_e32 v67, 16, v67
	v_add3_u32 v79, v91, v79, s51
	v_and_or_b32 v81, v79, s52, v67
	v_bfe_u32 v67, v93, 16, 1
	v_add3_u32 v67, v93, v67, s51
	v_bfe_u32 v79, v95, 16, 1
	v_lshrrev_b32_e32 v67, 16, v67
	v_add3_u32 v79, v95, v79, s51
	v_and_or_b32 v82, v79, s52, v67
	v_bfe_u32 v67, v97, 16, 1
	v_add3_u32 v67, v97, v67, s51
	v_bfe_u32 v79, v99, 16, 1
	v_lshrrev_b32_e32 v67, 16, v67
	v_add3_u32 v79, v99, v79, s51
	v_and_or_b32 v83, v79, s52, v67
	v_add_u32_e32 v67, s24, v70
	v_lshlrev_b32_e32 v79, 1, v67
	v_and_b32_e32 v84, 0x7f, v67
	v_and_or_b32 v79, v79, s53, v84
	v_cndmask_b32_e32 v67, v79, v67, vcc
	v_add_u32_e32 v67, s48, v67
	v_mad_u64_u32 v[84:85], s[18:19], v67, s47, 0
	v_ashrrev_i32_e32 v79, 31, v67
	v_mov_b32_e32 v86, v85
	v_mad_u64_u32 v[86:87], s[18:19], v79, s47, v[86:87]
	v_mov_b32_e32 v85, v86
	v_lshl_add_u64 v[84:85], v[84:85], 1, s[16:17]
	v_lshl_add_u64 v[84:85], v[84:85], 0, s[2:3]
	ds_read2_b32 v[86:87], v73 offset0:16 offset1:24
	v_lshl_add_u64 v[84:85], v[84:85], 0, v[68:69]
	global_store_dwordx4 v[84:85], v[80:83], off nt
	ds_read2_b32 v[84:85], v73 offset0:49 offset1:57
	ds_read2_b32 v[88:89], v73 offset0:82 offset1:90
	ds_read2_b32 v[90:91], v73 offset0:115 offset1:123
	s_waitcnt lgkmcnt(3)
; #define LAS __attribute__((address_space(3)))
; __device__ __forceinline__ unsigned pk2(float lo, float hi) { return f2bf(lo) | (f2bf(hi) << 16); }
;     __device__ __forceinline__ const float* x() const { return (const float*)ld(0); }
;     __device__ __forceinline__ const float* c() const { return (const float*)ld(1); }
; template <bool NT = true> __device__ __forceinline__ void cvt_store(const CvtItem& d, const f32x4 (&v)[8], LAS float* scr, int lane) {
;     const int rr = lane >> 3, c4 = (lane & 7) * 4;
; #pragma unroll
;     for (int q = 0; q < 8; ++q) { LAS float* t = scr + (8 * q + rr) * 33 + c4; t[0] = v[q].x; t[1] = v[q].y; t[2] = v[q].z; t[3] = v[q].w; }
;     asm volatile("s_waitcnt lgkmcnt(0)" ::: "memory");
;     const int c = lane & 7;
; #pragma unroll
;     for (int j = 0; j < 4; ++j) { const int n = (lane >> 3) + 8 * j; const LAS float* s = scr + (8 * c) * 33 + n;
;         u32x4 o; o.x = pk2(s[0 * 33], s[1 * 33]); o.y = pk2(s[2 * 33], s[3 * 33]); o.z = pk2(s[4 * 33], s[5 * 33]); o.w = pk2(s[6 * 33], s[7 * 33]);
;         const int ng = d.n0 + n, drow = d.row_off + (d.ilv ? ((ng >> 7) * 256 + (ng & 127)) : ng);
;         if (NT) __builtin_nontemporal_store(o, (u32x4*)(d.dst + (size_t)drow * d.K + d.k0 + 8 * c)); else *(u32x4*)(d.dst + (size_t)drow * d.K + d.k0 + 8 * c) = o; }
;     asm volatile("s_waitcnt lgkmcnt(0)" ::: "memory");
; __device__ __forceinline__ void convert_moe_items(const Ctx& a, int layer, LAS unsigned char* lds, int it0, int it1, int widx, int nw, int wave, int lane) {
;     ...
;         hb = (it + nw < it1);
;         if (hb) { db = decode(it + nw); cvt_load(db, vb, lane); }
	v_bfe_u32 v67, v86, 16, 1
	v_add3_u32 v67, v86, v67, s51
	s_waitcnt lgkmcnt(2)
	v_bfe_u32 v79, v84, 16, 1
	ds_read2_b32 v[92:93], v73 offset0:148 offset1:156
	v_lshrrev_b32_e32 v67, 16, v67
	v_add3_u32 v79, v84, v79, s51
	ds_read2_b32 v[94:95], v73 offset0:181 offset1:189
	v_and_or_b32 v80, v79, s52, v67
	s_waitcnt lgkmcnt(3)
	v_bfe_u32 v67, v88, 16, 1
	v_add3_u32 v67, v88, v67, s51
	s_waitcnt lgkmcnt(2)
	v_bfe_u32 v79, v90, 16, 1
	ds_read2_b32 v[96:97], v73 offset0:214 offset1:222
	v_lshrrev_b32_e32 v67, 16, v67
	v_add3_u32 v79, v90, v79, s51
	ds_read2_b32 v[98:99], v73 offset0:247 offset1:255
	v_and_or_b32 v81, v79, s52, v67
	s_waitcnt lgkmcnt(3)
	v_bfe_u32 v67, v92, 16, 1
	v_add3_u32 v67, v92, v67, s51
	s_waitcnt lgkmcnt(2)
	v_bfe_u32 v79, v94, 16, 1
	v_lshrrev_b32_e32 v67, 16, v67
	v_add3_u32 v79, v94, v79, s51
	v_and_or_b32 v82, v79, s52, v67
	s_waitcnt lgkmcnt(1)
	v_bfe_u32 v67, v96, 16, 1
	v_add3_u32 v67, v96, v67, s51
	s_waitcnt lgkmcnt(0)
	v_bfe_u32 v79, v98, 16, 1
	v_lshrrev_b32_e32 v67, 16, v67
	v_add3_u32 v79, v98, v79, s51
	v_and_or_b32 v83, v79, s52, v67
	v_add_u32_e32 v67, s24, v71
	v_lshlrev_b32_e32 v79, 1, v67
	v_and_b32_e32 v84, 0x7f, v67
	v_and_or_b32 v79, v79, s53, v84
	v_cndmask_b32_e32 v67, v79, v67, vcc
	v_add_u32_e32 v67, s48, v67
	v_mad_u64_u32 v[100:101], s[18:19], v67, s47, 0
	v_ashrrev_i32_e32 v79, 31, v67
	v_mov_b32_e32 v84, v101
	v_mad_u64_u32 v[102:103], s[18:19], v79, s47, v[84:85]
	v_mov_b32_e32 v101, v102
	v_lshl_add_u64 v[100:101], v[100:101], 1, s[16:17]
	v_bfe_u32 v67, v87, 16, 1
	v_lshl_add_u64 v[100:101], v[100:101], 0, s[2:3]
	v_add3_u32 v67, v87, v67, s51
	v_bfe_u32 v79, v85, 16, 1
	v_lshl_add_u64 v[100:101], v[100:101], 0, v[68:69]
	v_lshrrev_b32_e32 v67, 16, v67
	v_add3_u32 v79, v85, v79, s51
	global_store_dwordx4 v[100:101], v[80:83], off nt
	s_nop 1
	v_and_or_b32 v80, v79, s52, v67
	v_bfe_u32 v67, v89, 16, 1
	v_add3_u32 v67, v89, v67, s51
	v_bfe_u32 v79, v91, 16, 1
	v_lshrrev_b32_e32 v67, 16, v67
	v_add3_u32 v79, v91, v79, s51
	v_and_or_b32 v81, v79, s52, v67
	v_bfe_u32 v67, v93, 16, 1
	v_add3_u32 v67, v93, v67, s51
	v_bfe_u32 v79, v95, 16, 1
	v_lshrrev_b32_e32 v67, 16, v67
	v_add3_u32 v79, v95, v79, s51
	v_and_or_b32 v82, v79, s52, v67
	v_bfe_u32 v67, v97, 16, 1
	v_add3_u32 v67, v97, v67, s51
	v_bfe_u32 v79, v99, 16, 1
	v_lshrrev_b32_e32 v67, 16, v67
	v_add3_u32 v79, v99, v79, s51
	v_and_or_b32 v83, v79, s52, v67
	v_add_u32_e32 v67, s24, v72
	v_lshlrev_b32_e32 v79, 1, v67
	v_and_b32_e32 v84, 0x7f, v67
	v_and_or_b32 v79, v79, s53, v84
	v_cndmask_b32_e32 v67, v79, v67, vcc
	v_add_u32_e32 v67, s48, v67
	v_mad_u64_u32 v[84:85], s[18:19], v67, s47, 0
	v_ashrrev_i32_e32 v79, 31, v67
	v_mov_b32_e32 v86, v85
	v_mad_u64_u32 v[86:87], s[18:19], v79, s47, v[86:87]
	v_mov_b32_e32 v85, v86
	v_lshl_add_u64 v[84:85], v[84:85], 1, s[16:17]
	v_lshl_add_u64 v[84:85], v[84:85], 0, s[2:3]
	v_lshl_add_u64 v[84:85], v[84:85], 0, v[68:69]
	global_store_dwordx4 v[84:85], v[80:83], off nt
	s_add_i32 s2, s50, s41
	s_waitcnt lgkmcnt(0)
	s_cmp_lt_i32 s2, 0x9800
	s_cselect_b64 s[18:19], -1, 0
	s_cmp_gt_i32 s2, 0x97ff
	s_cbranch_scc1 .LBB0_676
	s_mul_hi_i32 s3, s2, 0x2aaaaaab
	s_lshr_b32 s13, s3, 31
	s_ashr_i32 s3, s3, 9
	s_add_i32 s16, s3, s13
	s_mul_i32 s3, s16, 0xc00
	s_ashr_i32 s17, s16, 31
	s_sub_i32 s15, s2, s3
	s_lshl_b64 s[2:3], s[16:17], 21
	s_add_u32 s22, s2, 0x2000000
	s_addc_u32 s23, s3, 0
	s_lshl_b32 s28, s16, 11
	s_cmpk_gt_i32 s15, 0x3ff
	s_mov_b64 s[24:25], -1
	s_cbranch_scc0 .LBB0_694
	s_cmpk_gt_u32 s15, 0x7ff
	s_mov_b64 s[16:17], -1
	s_cbranch_scc0 .LBB0_692
	s_add_i32 s13, s15, 0xfffff800
	s_lshl_b64 s[2:3], s[22:23], 2
	s_add_u32 s2, s38, s2
	s_addc_u32 s3, s37, s3
	s_mov_b64 s[16:17], 0

; __device__ __forceinline__ void convert_moe_items(const Ctx& a, int layer, LAS unsigned char* lds, int it0, int it1, int widx, int nw, int wave, int lane) {
;     ...
;     int it = it0 + widx;
;     if (it >= it1) return;
;     f32x4 va[8], vb[8]; CvtItem da = decode(it), db = da; bool hb = (it + nw < it1);
; PHASE_FN ph_wout(unsigned* dep, const XcdBarrier& bar) { PH_PRO;
;     ...
;         pg8::gemm_phase<pg8::EpiResid<true>, pg8::StaticOrder, true, true>(lds, g, S, E);
;         if (GH == G) convert_moe_items(a, 1, lds, 0, L1_A, gw, NGW, wave, lane);
.LBB0_741:
	s_cmp_lg_u32 s43, s45
	s_cbranch_scc1 .LBB0_791
	s_add_i32 s1, 0, 0x23f10
	v_mov_b32_e32 v2, s1
	s_waitcnt vmcnt(6)
	ds_read_b64 v[6:7], v2
	s_lshl_b32 s0, s96, 3
	s_add_i32 s37, s44, s0
	s_add_i32 s0, 0, 0x23ee8
	v_mov_b32_e32 v2, s0
	s_add_i32 s0, 0, 0x23ef8
	s_waitcnt lgkmcnt(0)
	v_readfirstlane_b32 s3, v6
	v_mov_b32_e32 v6, s0
	ds_read2_b64 v[2:5], v2 offset1:1
	v_readfirstlane_b32 s2, v7
	ds_read_b64 v[6:7], v6
	s_cmp_gt_i32 s37, 0x97ff
	s_waitcnt lgkmcnt(1)
	v_readfirstlane_b32 s28, v3
	v_readfirstlane_b32 s29, v2
	v_readfirstlane_b32 s30, v5
	v_readfirstlane_b32 s31, v4
	s_waitcnt lgkmcnt(0)
	v_readfirstlane_b32 s33, v7
	v_readfirstlane_b32 s34, v6
	s_cbranch_scc1 .LBB0_791
	s_add_u32 s0, s3, 0xa530000
	s_addc_u32 s1, s2, 0
	s_add_u32 s4, s3, 0x16530000
	s_addc_u32 s5, s2, 0
	s_mul_hi_i32 s2, s37, 0x2aaaaaab
	s_lshr_b32 s3, s2, 31
	s_ashr_i32 s2, s2, 9
	s_add_i32 s2, s2, s3
	s_mul_i32 s3, s2, 0xc00
	s_sub_i32 s15, s37, s3
	s_ashr_i32 s3, s2, 31
	s_lshl_b64 s[6:7], s[2:3], 21
	s_add_u32 s10, s6, 0x2000000
	s_addc_u32 s11, s7, 0
	s_lshl_b32 s17, s2, 11
	s_cmpk_gt_i32 s15, 0x3ff
	s_cbranch_scc0 .LBB0_746
	s_cmpk_gt_u32 s15, 0x7ff
	s_cbranch_scc0 .LBB0_747
	s_add_i32 s16, s15, 0xfffff800
	s_lshl_b64 s[2:3], s[10:11], 2
	s_add_u32 s2, s34, s2
	s_addc_u32 s3, s33, s3
	s_mov_b64 s[6:7], 0
	s_branch .LBB0_748

; __device__ __forceinline__ void cvt_load(const CvtItem& d, f32x4 (&v)[8], int lane) {
;     const float* p = d.src + (size_t)(d.k0 + (lane >> 3)) * d.N + d.n0 + (lane & 7) * 4;
; #pragma unroll
;     for (int q = 0; q < 8; ++q) v[q] = __builtin_nontemporal_load((const f32x4*)(p + (size_t)(8 * q) * d.N));
; }
; __device__ __forceinline__ void convert_moe_items(const Ctx& a, int layer, LAS unsigned char* lds, int it0, int it1, int widx, int nw, int wave, int lane) {
;     ...
;     f32x4 va[8], vb[8]; CvtItem da = decode(it), db = da; bool hb = (it + nw < it1);
;     cvt_load(da, va, lane);
;     if (hb) { db = decode(it + nw); cvt_load(db, vb, lane); }
.LBB0_754:
	s_lshr_b32 s12, s14, 5
	v_cvt_f32_i32_e32 v2, s12
	s_sext_i32_i16 s10, s16
	v_cvt_f32_i32_e32 v3, s10
	s_ashr_i32 s10, s10, 30
	v_rcp_iflag_f32_e32 v4, v2
	s_or_b32 s13, s10, 1
	v_lshrrev_b32_e32 v70, 3, v214
	v_and_b32_e32 v1, 28, v1
	v_mul_f32_e32 v4, v3, v4
	v_trunc_f32_e32 v4, v4
	v_fma_f32 v3, -v4, v2, v3
	v_cvt_i32_f32_e32 v4, v4
	v_cmp_ge_f32_e64 s[10:11], |v3|, v2
	s_and_b64 s[10:11], s[10:11], exec
	s_cselect_b32 s10, s13, 0
	v_readfirstlane_b32 s11, v4
	s_add_i32 s11, s11, s10
	s_sext_i32_i16 s10, s11
	s_mul_i32 s11, s11, s12
	s_sub_i32 s11, s16, s11
	s_lshl_b32 s10, s10, 6
	s_sext_i32_i16 s11, s11
	s_lshl_b32 s12, s11, 5
	s_add_i32 s11, s42, s37
	v_or_b32_e32 v2, s10, v70
	s_cmp_lt_i32 s11, 0x9800
	v_mul_hi_i32_i24_e32 v3, s14, v2
	v_mul_i32_i24_e32 v2, s14, v2
	s_cselect_b64 s[16:17], -1, 0
	s_ashr_i32 s13, s12, 31
	v_lshl_add_u64 v[2:3], v[2:3], 2, s[2:3]
	s_mov_b32 s15, 0
	v_lshl_add_u64 v[2:3], s[12:13], 2, v[2:3]
	v_mov_b32_e32 v67, 0
	v_lshlrev_b32_e32 v66, 2, v1
	s_lshl_b64 s[18:19], s[14:15], 5
	s_waitcnt vmcnt(5)
	v_lshl_add_u64 v[10:11], v[2:3], 0, v[66:67]
	v_lshl_add_u64 v[12:13], v[10:11], 0, s[18:19]
	s_waitcnt vmcnt(3)
	v_lshl_add_u64 v[18:19], v[12:13], 0, s[18:19]
	v_lshl_add_u64 v[20:21], v[18:19], 0, s[18:19]
	s_waitcnt vmcnt(1)
	v_lshl_add_u64 v[26:27], v[20:21], 0, s[18:19]
	v_lshl_add_u64 v[28:29], v[26:27], 0, s[18:19]
	v_lshl_add_u64 v[34:35], v[28:29], 0, s[18:19]
	global_load_dwordx4 v[2:5], v[10:11], off nt
	global_load_dwordx4 v[6:9], v[12:13], off nt
	s_nop 0
	global_load_dwordx4 v[10:13], v[18:19], off nt
	global_load_dwordx4 v[14:17], v[20:21], off nt
	s_nop 0
	global_load_dwordx4 v[18:21], v[26:27], off nt
	global_load_dwordx4 v[22:25], v[28:29], off nt
	v_lshl_add_u64 v[36:37], v[34:35], 0, s[18:19]
	global_load_dwordx4 v[26:29], v[34:35], off nt
	global_load_dwordx4 v[30:33], v[36:37], off nt
	s_cmp_gt_i32 s11, 0x97ff
	s_mov_b64 s[14:15], s[6:7]
	s_mov_b32 s39, s35
	s_mov_b32 s40, s36
	s_mov_b32 s38, s27
	s_mov_b32 s20, s10
	s_mov_b32 s22, s12
	s_cbranch_scc1 .LBB0_767
	s_mul_hi_i32 s2, s11, 0x2aaaaaab
	s_lshr_b32 s3, s2, 31
	s_ashr_i32 s2, s2, 9
	s_add_i32 s2, s2, s3
	s_mul_i32 s3, s2, 0xc00
	s_sub_i32 s13, s11, s3
	s_ashr_i32 s3, s2, 31
	s_lshl_b64 s[14:15], s[2:3], 21
	s_add_u32 s20, s14, 0x2000000
	s_addc_u32 s21, s15, 0
	s_lshl_b32 s19, s2, 11
	s_cmpk_gt_i32 s13, 0x3ff
	s_cbranch_scc0 .LBB0_758
	s_cmpk_gt_u32 s13, 0x7ff
	s_cbranch_scc0 .LBB0_759
	s_add_i32 s11, s13, 0xfffff800
	s_lshl_b64 s[2:3], s[20:21], 2
	s_add_u32 s2, s34, s2
	s_addc_u32 s3, s33, s3
	s_mov_b64 s[14:15], 0
	s_branch .LBB0_760

; #define LAS __attribute__((address_space(3)))
; __device__ __forceinline__ unsigned pk2(float lo, float hi) { return f2bf(lo) | (f2bf(hi) << 16); }
;     __device__ __forceinline__ const float* x() const { return (const float*)ld(0); }
;     __device__ __forceinline__ const float* c() const { return (const float*)ld(1); }
; template <bool NT = true> __device__ __forceinline__ void cvt_store(const CvtItem& d, const f32x4 (&v)[8], LAS float* scr, int lane) {
;     const int rr = lane >> 3, c4 = (lane & 7) * 4;
; #pragma unroll
;     for (int q = 0; q < 8; ++q) { LAS float* t = scr + (8 * q + rr) * 33 + c4; t[0] = v[q].x; t[1] = v[q].y; t[2] = v[q].z; t[3] = v[q].w; }
;     asm volatile("s_waitcnt lgkmcnt(0)" ::: "memory");
;     const int c = lane & 7;
; #pragma unroll
;     for (int j = 0; j < 4; ++j) { const int n = (lane >> 3) + 8 * j; const LAS float* s = scr + (8 * c) * 33 + n;
;         u32x4 o; o.x = pk2(s[0 * 33], s[1 * 33]); o.y = pk2(s[2 * 33], s[3 * 33]); o.z = pk2(s[4 * 33], s[5 * 33]); o.w = pk2(s[6 * 33], s[7 * 33]);
;         const int ng = d.n0 + n, drow = d.row_off + (d.ilv ? ((ng >> 7) * 256 + (ng & 127)) : ng);
;         if (NT) __builtin_nontemporal_store(o, (u32x4*)(d.dst + (size_t)drow * d.K + d.k0 + 8 * c)); else *(u32x4*)(d.dst + (size_t)drow * d.K + d.k0 + 8 * c) = o; }
;     asm volatile("s_waitcnt lgkmcnt(0)" ::: "memory");
; __device__ __forceinline__ void convert_moe_items(const Ctx& a, int layer, LAS unsigned char* lds, int it0, int it1, int widx, int nw, int wave, int lane) {
;     ...
;         cvt_store(da, va, scr, lane);
;         it += 2 * nw; const bool ha = (it < it1);
;         if (ha) { da = decode(it); cvt_load(da, va, lane); }
.LBB0_771:
	v_add_u32_e32 v79, 0x420, v74
	v_add_u32_e32 v80, 0x428, v74
	v_add_u32_e32 v81, 0x840, v74
	v_add_u32_e32 v82, 0x848, v74
	v_add_u32_e32 v83, 0xc60, v74
	v_add_u32_e32 v84, 0xc68, v74
	v_add_u32_e32 v85, 0x1080, v74
	v_add_u32_e32 v86, 0x1088, v74
	v_add_u32_e32 v87, 0x14a0, v74
	v_add_u32_e32 v88, 0x14a8, v74
	v_add_u32_e32 v89, 0x18c0, v74
	v_add_u32_e32 v90, 0x18c8, v74
	v_add_u32_e32 v91, 0x1ce0, v74
	v_add_u32_e32 v92, 0x1ce8, v74
	s_waitcnt vmcnt(7)
	ds_write2_b32 v74, v2, v3 offset1:1
	ds_write2_b32 v74, v4, v5 offset0:2 offset1:3
	s_waitcnt vmcnt(6)
	ds_write2_b32 v79, v6, v7 offset1:1
	ds_write2_b32 v80, v8, v9 offset1:1
	s_waitcnt vmcnt(5)
	ds_write2_b32 v81, v10, v11 offset1:1
	ds_write2_b32 v82, v12, v13 offset1:1
	s_waitcnt vmcnt(4)
	ds_write2_b32 v83, v14, v15 offset1:1
	ds_write2_b32 v84, v16, v17 offset1:1
	s_waitcnt vmcnt(3)
	ds_write2_b32 v85, v18, v19 offset1:1
	ds_write2_b32 v86, v20, v21 offset1:1
	s_waitcnt vmcnt(2)
	ds_write2_b32 v87, v22, v23 offset1:1
	ds_write2_b32 v88, v24, v25 offset1:1
	s_waitcnt vmcnt(1)
	ds_write2_b32 v89, v26, v27 offset1:1
	ds_write2_b32 v90, v28, v29 offset1:1
	s_waitcnt vmcnt(0)
	ds_write2_b32 v91, v30, v31 offset1:1
	ds_write2_b32 v92, v32, v33 offset1:1
	s_waitcnt lgkmcnt(0)
	ds_read2_b32 v[98:99], v73 offset1:8
	ds_read2_b32 v[100:101], v73 offset0:33 offset1:41
	ds_read2_b32 v[102:103], v73 offset0:66 offset1:74
	ds_read2_b32 v[104:105], v73 offset0:99 offset1:107
	ds_read2_b32 v[106:107], v73 offset0:132 offset1:140
	s_waitcnt lgkmcnt(4)
	v_bfe_u32 v67, v98, 16, 1
	v_add3_u32 v67, v98, v67, s43
	s_waitcnt lgkmcnt(3)
	v_bfe_u32 v93, v100, 16, 1
	v_lshrrev_b32_e32 v67, 16, v67
	v_add3_u32 v93, v100, v93, s43
	ds_read2_b32 v[108:109], v73 offset0:165 offset1:173
	v_and_or_b32 v94, v93, s44, v67
	s_waitcnt lgkmcnt(3)
	v_bfe_u32 v67, v102, 16, 1
	v_add3_u32 v67, v102, v67, s43
	s_waitcnt lgkmcnt(2)
	v_bfe_u32 v93, v104, 16, 1
	ds_read2_b32 v[110:111], v73 offset0:198 offset1:206
	v_lshrrev_b32_e32 v67, 16, v67
	v_add3_u32 v93, v104, v93, s43
	ds_read2_b32 v[112:113], v73 offset0:231 offset1:239
	v_and_or_b32 v95, v93, s44, v67
	s_waitcnt lgkmcnt(3)
	v_bfe_u32 v67, v106, 16, 1
	v_add3_u32 v67, v106, v67, s43
	s_waitcnt lgkmcnt(2)
	v_bfe_u32 v93, v108, 16, 1
	v_lshrrev_b32_e32 v67, 16, v67
	v_add3_u32 v93, v108, v93, s43
	v_and_or_b32 v96, v93, s44, v67
	s_waitcnt lgkmcnt(1)
	v_bfe_u32 v67, v110, 16, 1
	v_add3_u32 v67, v110, v67, s43
	s_waitcnt lgkmcnt(0)
	v_bfe_u32 v93, v112, 16, 1
	s_cmp_eq_u32 s27, 0
	v_lshrrev_b32_e32 v67, 16, v67
	v_add3_u32 v93, v112, v93, s43
	s_cselect_b64 vcc, -1, 0
	s_lshl_b32 s2, s12, 1
	v_and_or_b32 v97, v93, s44, v67
	s_and_b32 s13, s2, 0xffffff00
	v_bitop3_b32 v93, s12, v75, v70 bitop3:0xc8
	v_or_b32_e32 v67, s12, v70
	v_or_b32_e32 v93, s13, v93
	v_cndmask_b32_e32 v67, v93, v67, vcc
	v_add_u32_e32 v67, s36, v67
	v_mad_u64_u32 v[114:115], s[2:3], v67, s35, 0
	v_ashrrev_i32_e32 v93, 31, v67
	v_mov_b32_e32 v98, v115
	v_mad_u64_u32 v[116:117], s[2:3], v93, s35, v[98:99]
	v_mov_b32_e32 v115, v116
	s_ashr_i32 s11, s10, 31
	v_lshl_add_u64 v[114:115], v[114:115], 1, s[6:7]
	s_lshl_b64 s[2:3], s[10:11], 1
	v_bfe_u32 v67, v99, 16, 1
	v_lshl_add_u64 v[114:115], v[114:115], 0, s[2:3]
	v_add3_u32 v67, v99, v67, s43
	v_bfe_u32 v93, v101, 16, 1
	v_lshl_add_u64 v[114:115], v[114:115], 0, v[68:69]
	v_lshrrev_b32_e32 v67, 16, v67
	v_add3_u32 v93, v101, v93, s43
	global_store_dwordx4 v[114:115], v[94:97], off nt
	s_add_i32 s46, s37, s41
	s_cmp_gt_i32 s46, 0x97ff
	v_and_or_b32 v94, v93, s44, v67
	v_bfe_u32 v67, v103, 16, 1
	v_add3_u32 v67, v103, v67, s43
	v_bfe_u32 v93, v105, 16, 1
	v_lshrrev_b32_e32 v67, 16, v67
	v_add3_u32 v93, v105, v93, s43
	v_and_or_b32 v95, v93, s44, v67
	v_bfe_u32 v67, v107, 16, 1
	v_add3_u32 v67, v107, v67, s43
	v_bfe_u32 v93, v109, 16, 1
	v_lshrrev_b32_e32 v67, 16, v67
	v_add3_u32 v93, v109, v93, s43
	v_and_or_b32 v96, v93, s44, v67
	v_bfe_u32 v67, v111, 16, 1
	v_add3_u32 v67, v111, v67, s43
	v_bfe_u32 v93, v113, 16, 1
	v_lshrrev_b32_e32 v67, 16, v67
	v_add3_u32 v93, v113, v93, s43
	v_and_or_b32 v97, v93, s44, v67
	v_bitop3_b32 v93, s12, v76, v1 bitop3:0xc8
	v_or_b32_e32 v67, s12, v1
	v_or_b32_e32 v93, s13, v93
	v_cndmask_b32_e32 v67, v93, v67, vcc
	v_add_u32_e32 v67, s36, v67
	v_mad_u64_u32 v[98:99], s[24:25], v67, s35, 0
	v_ashrrev_i32_e32 v93, 31, v67
	v_mov_b32_e32 v100, v99
	v_mad_u64_u32 v[100:101], s[24:25], v93, s35, v[100:101]
	v_mov_b32_e32 v99, v100
	v_lshl_add_u64 v[98:99], v[98:99], 1, s[6:7]
	v_lshl_add_u64 v[98:99], v[98:99], 0, s[2:3]
	ds_read2_b32 v[100:101], v73 offset0:16 offset1:24
	v_lshl_add_u64 v[98:99], v[98:99], 0, v[68:69]
	global_store_dwordx4 v[98:99], v[94:97], off nt
	ds_read2_b32 v[98:99], v73 offset0:49 offset1:57
	ds_read2_b32 v[102:103], v73 offset0:82 offset1:90
	ds_read2_b32 v[104:105], v73 offset0:115 offset1:123
	s_waitcnt lgkmcnt(3)
; #define LAS __attribute__((address_space(3)))
; __device__ __forceinline__ unsigned pk2(float lo, float hi) { return f2bf(lo) | (f2bf(hi) << 16); }
;     __device__ __forceinline__ const float* x() const { return (const float*)ld(0); }
;     __device__ __forceinline__ const float* c() const { return (const float*)ld(1); }
; template <bool NT = true> __device__ __forceinline__ void cvt_store(const CvtItem& d, const f32x4 (&v)[8], LAS float* scr, int lane) {
;     const int rr = lane >> 3, c4 = (lane & 7) * 4;
; #pragma unroll
;     for (int q = 0; q < 8; ++q) { LAS float* t = scr + (8 * q + rr) * 33 + c4; t[0] = v[q].x; t[1] = v[q].y; t[2] = v[q].z; t[3] = v[q].w; }
;     asm volatile("s_waitcnt lgkmcnt(0)" ::: "memory");
;     const int c = lane & 7;
; #pragma unroll
;     for (int j = 0; j < 4; ++j) { const int n = (lane >> 3) + 8 * j; const LAS float* s = scr + (8 * c) * 33 + n;
;         u32x4 o; o.x = pk2(s[0 * 33], s[1 * 33]); o.y = pk2(s[2 * 33], s[3 * 33]); o.z = pk2(s[4 * 33], s[5 * 33]); o.w = pk2(s[6 * 33], s[7 * 33]);
;         const int ng = d.n0 + n, drow = d.row_off + (d.ilv ? ((ng >> 7) * 256 + (ng & 127)) : ng);
;         if (NT) __builtin_nontemporal_store(o, (u32x4*)(d.dst + (size_t)drow * d.K + d.k0 + 8 * c)); else *(u32x4*)(d.dst + (size_t)drow * d.K + d.k0 + 8 * c) = o; }
;     asm volatile("s_waitcnt lgkmcnt(0)" ::: "memory");
; __device__ __forceinline__ void convert_moe_items(const Ctx& a, int layer, LAS unsigned char* lds, int it0, int it1, int widx, int nw, int wave, int lane) {
;     ...
;     auto decode = [&](int it) { CvtItem d; const int e = it / PER_E; int r = it % PER_E; const size_t eo = ((size_t)layer * NE + e) * (size_t)DM * FE;
;         if (r < I_G)          { d.src = wg + eo; d.dst = WGU; d.N = FE; d.K = DM; d.row_off = e * 2048; d.ilv = 1; }
;         else if (r < 2 * I_G) { r -= I_G; d.src = wu + eo; d.dst = WGU; d.N = FE; d.K = DM; d.row_off = e * 2048 + 128; d.ilv = 1; }
;         else                  { r -= 2 * I_G; d.src = wd + eo; d.dst = WD; d.N = DM; d.K = FE; d.row_off = e * 2048; d.ilv = 0; }
;         const int nblk = d.N / 32; d.k0 = 64 * (r / nblk); d.n0 = 32 * (r % nblk); return d; };
	v_bfe_u32 v67, v100, 16, 1
	v_add3_u32 v67, v100, v67, s43
	s_waitcnt lgkmcnt(2)
	v_bfe_u32 v93, v98, 16, 1
	ds_read2_b32 v[106:107], v73 offset0:148 offset1:156
	v_lshrrev_b32_e32 v67, 16, v67
	v_add3_u32 v93, v98, v93, s43
	ds_read2_b32 v[108:109], v73 offset0:181 offset1:189
	v_and_or_b32 v94, v93, s44, v67
	s_waitcnt lgkmcnt(3)
	v_bfe_u32 v67, v102, 16, 1
	v_add3_u32 v67, v102, v67, s43
	s_waitcnt lgkmcnt(2)
	v_bfe_u32 v93, v104, 16, 1
	ds_read2_b32 v[110:111], v73 offset0:214 offset1:222
	v_lshrrev_b32_e32 v67, 16, v67
	v_add3_u32 v93, v104, v93, s43
	ds_read2_b32 v[112:113], v73 offset0:247 offset1:255
	v_and_or_b32 v95, v93, s44, v67
	s_waitcnt lgkmcnt(3)
	v_bfe_u32 v67, v106, 16, 1
	v_add3_u32 v67, v106, v67, s43
	s_waitcnt lgkmcnt(2)
	v_bfe_u32 v93, v108, 16, 1
	v_lshrrev_b32_e32 v67, 16, v67
	v_add3_u32 v93, v108, v93, s43
	v_and_or_b32 v96, v93, s44, v67
	s_waitcnt lgkmcnt(1)
	v_bfe_u32 v67, v110, 16, 1
	v_add3_u32 v67, v110, v67, s43
	s_waitcnt lgkmcnt(0)
	v_bfe_u32 v93, v112, 16, 1
	v_lshrrev_b32_e32 v67, 16, v67
	v_add3_u32 v93, v112, v93, s43
	v_and_or_b32 v97, v93, s44, v67
	v_bitop3_b32 v93, s12, v77, v71 bitop3:0xc8
	v_or_b32_e32 v67, s12, v71
	v_or_b32_e32 v93, s13, v93
	v_cndmask_b32_e32 v67, v93, v67, vcc
	v_add_u32_e32 v67, s36, v67
	v_mad_u64_u32 v[114:115], s[24:25], v67, s35, 0
	v_ashrrev_i32_e32 v93, 31, v67
	v_mov_b32_e32 v98, v115
	v_mad_u64_u32 v[116:117], s[24:25], v93, s35, v[98:99]
	v_mov_b32_e32 v115, v116
	v_lshl_add_u64 v[114:115], v[114:115], 1, s[6:7]
	v_bfe_u32 v67, v101, 16, 1
	v_lshl_add_u64 v[114:115], v[114:115], 0, s[2:3]
	v_add3_u32 v67, v101, v67, s43
	v_bfe_u32 v93, v99, 16, 1
	v_lshl_add_u64 v[114:115], v[114:115], 0, v[68:69]
	v_lshrrev_b32_e32 v67, 16, v67
	v_add3_u32 v93, v99, v93, s43
	global_store_dwordx4 v[114:115], v[94:97], off nt
	s_nop 1
	v_and_or_b32 v94, v93, s44, v67
	v_bfe_u32 v67, v103, 16, 1
	v_add3_u32 v67, v103, v67, s43
	v_bfe_u32 v93, v105, 16, 1
	v_lshrrev_b32_e32 v67, 16, v67
	v_add3_u32 v93, v105, v93, s43
	v_and_or_b32 v95, v93, s44, v67
	v_bfe_u32 v67, v107, 16, 1
	v_add3_u32 v67, v107, v67, s43
	v_bfe_u32 v93, v109, 16, 1
	v_lshrrev_b32_e32 v67, 16, v67
	v_add3_u32 v93, v109, v93, s43
	v_and_or_b32 v96, v93, s44, v67
	v_bfe_u32 v67, v111, 16, 1
	v_add3_u32 v67, v111, v67, s43
	v_bfe_u32 v93, v113, 16, 1
	v_lshrrev_b32_e32 v67, 16, v67
	v_add3_u32 v93, v113, v93, s43
	v_and_or_b32 v97, v93, s44, v67
	v_bitop3_b32 v93, s12, v78, v72 bitop3:0xc8
	v_or_b32_e32 v67, s12, v72
	v_or_b32_e32 v93, s13, v93
	v_cndmask_b32_e32 v67, v93, v67, vcc
	v_add_u32_e32 v67, s36, v67
	v_mad_u64_u32 v[98:99], s[24:25], v67, s35, 0
	v_ashrrev_i32_e32 v93, 31, v67
	v_mov_b32_e32 v100, v99
	v_mad_u64_u32 v[100:101], s[24:25], v93, s35, v[100:101]
	v_mov_b32_e32 v99, v100
	v_lshl_add_u64 v[98:99], v[98:99], 1, s[6:7]
	v_lshl_add_u64 v[98:99], v[98:99], 0, s[2:3]
	v_lshl_add_u64 v[98:99], v[98:99], 0, v[68:69]
	global_store_dwordx4 v[98:99], v[94:97], off nt
	s_waitcnt lgkmcnt(0)
	s_cselect_b64 s[24:25], -1, 0
	s_and_b64 vcc, exec, s[24:25]
	s_cbranch_vccnz .LBB0_780
	s_mul_hi_i32 s2, s46, 0x2aaaaaab
	s_lshr_b32 s3, s2, 31
	s_ashr_i32 s2, s2, 9
	s_add_i32 s26, s2, s3
	s_mul_i32 s2, s26, 0xfffff400
	s_ashr_i32 s27, s26, 31
	s_add_i32 s21, s46, s2
	s_lshl_b64 s[2:3], s[26:27], 21
	s_add_u32 s10, s2, 0x2000000
	s_addc_u32 s11, s3, 0
	s_lshl_b32 s47, s26, 11
	s_cmpk_gt_i32 s21, 0x3ff
	s_mov_b64 s[12:13], -1
	s_cbranch_scc0 .LBB0_777
	s_mul_i32 s2, s26, 0xc00
	s_sub_i32 s12, s46, s2
	s_cmpk_gt_u32 s21, 0x7ff
	s_mov_b64 s[6:7], -1
	s_cbranch_scc0 .LBB0_775
	s_add_i32 s23, s12, 0xfffff800
	s_lshl_b64 s[2:3], s[10:11], 2
	s_add_u32 s2, s34, s2
	s_addc_u32 s3, s33, s3
	s_mov_b64 s[6:7], 0

; #define LAS __attribute__((address_space(3)))
; __device__ __forceinline__ unsigned pk2(float lo, float hi) { return f2bf(lo) | (f2bf(hi) << 16); }
;     __device__ __forceinline__ const float* x() const { return (const float*)ld(0); }
;     __device__ __forceinline__ const float* c() const { return (const float*)ld(1); }
; template <bool NT = true> __device__ __forceinline__ void cvt_store(const CvtItem& d, const f32x4 (&v)[8], LAS float* scr, int lane) {
;     const int rr = lane >> 3, c4 = (lane & 7) * 4;
; #pragma unroll
;     for (int q = 0; q < 8; ++q) { LAS float* t = scr + (8 * q + rr) * 33 + c4; t[0] = v[q].x; t[1] = v[q].y; t[2] = v[q].z; t[3] = v[q].w; }
;     asm volatile("s_waitcnt lgkmcnt(0)" ::: "memory");
;     const int c = lane & 7;
; #pragma unroll
;     for (int j = 0; j < 4; ++j) { const int n = (lane >> 3) + 8 * j; const LAS float* s = scr + (8 * c) * 33 + n;
;         u32x4 o; o.x = pk2(s[0 * 33], s[1 * 33]); o.y = pk2(s[2 * 33], s[3 * 33]); o.z = pk2(s[4 * 33], s[5 * 33]); o.w = pk2(s[6 * 33], s[7 * 33]);
;         const int ng = d.n0 + n, drow = d.row_off + (d.ilv ? ((ng >> 7) * 256 + (ng & 127)) : ng);
;         if (NT) __builtin_nontemporal_store(o, (u32x4*)(d.dst + (size_t)drow * d.K + d.k0 + 8 * c)); else *(u32x4*)(d.dst + (size_t)drow * d.K + d.k0 + 8 * c) = o; }
;     asm volatile("s_waitcnt lgkmcnt(0)" ::: "memory");
; __device__ __forceinline__ void convert_moe_items(const Ctx& a, int layer, LAS unsigned char* lds, int it0, int it1, int widx, int nw, int wave, int lane) {
;     ...
;         cvt_store(db, vb, scr, lane);
.LBB0_781:
	ds_write2_b32 v74, v34, v35 offset1:1
	ds_write2_b32 v74, v36, v37 offset0:2 offset1:3
	ds_write2_b32 v79, v38, v39 offset1:1
	ds_write2_b32 v80, v40, v41 offset1:1
	ds_write2_b32 v81, v42, v43 offset1:1
	ds_write2_b32 v82, v44, v45 offset1:1
	ds_write2_b32 v83, v46, v47 offset1:1
	ds_write2_b32 v84, v48, v49 offset1:1
	ds_write2_b32 v85, v50, v51 offset1:1
	ds_write2_b32 v86, v52, v53 offset1:1
	ds_write2_b32 v87, v54, v55 offset1:1
	ds_write2_b32 v88, v56, v57 offset1:1
	ds_write2_b32 v89, v58, v59 offset1:1
	ds_write2_b32 v90, v60, v61 offset1:1
	ds_write2_b32 v91, v62, v63 offset1:1
	ds_write2_b32 v92, v64, v65 offset1:1
	s_waitcnt lgkmcnt(0)
	ds_read2_b32 v[84:85], v73 offset1:8
	ds_read2_b32 v[86:87], v73 offset0:33 offset1:41
	ds_read2_b32 v[88:89], v73 offset0:66 offset1:74
	ds_read2_b32 v[90:91], v73 offset0:99 offset1:107
	ds_read2_b32 v[92:93], v73 offset0:132 offset1:140
	s_waitcnt lgkmcnt(4)
	v_bfe_u32 v67, v84, 16, 1
	v_add3_u32 v67, v84, v67, s43
	s_waitcnt lgkmcnt(3)
	v_bfe_u32 v79, v86, 16, 1
	v_lshrrev_b32_e32 v67, 16, v67
	v_add3_u32 v79, v86, v79, s43
	ds_read2_b32 v[94:95], v73 offset0:165 offset1:173
	v_and_or_b32 v80, v79, s44, v67
	s_waitcnt lgkmcnt(3)
	v_bfe_u32 v67, v88, 16, 1
	v_add3_u32 v67, v88, v67, s43
	s_waitcnt lgkmcnt(2)
	v_bfe_u32 v79, v90, 16, 1
	ds_read2_b32 v[96:97], v73 offset0:198 offset1:206
	v_lshrrev_b32_e32 v67, 16, v67
	v_add3_u32 v79, v90, v79, s43
	ds_read2_b32 v[98:99], v73 offset0:231 offset1:239
	v_and_or_b32 v81, v79, s44, v67
	s_waitcnt lgkmcnt(3)
	v_bfe_u32 v67, v92, 16, 1
	v_add3_u32 v67, v92, v67, s43
	s_waitcnt lgkmcnt(2)
	v_bfe_u32 v79, v94, 16, 1
	v_lshrrev_b32_e32 v67, 16, v67
	v_add3_u32 v79, v94, v79, s43
	v_and_or_b32 v82, v79, s44, v67
	s_waitcnt lgkmcnt(1)
	v_bfe_u32 v67, v96, 16, 1
	v_add3_u32 v67, v96, v67, s43
	s_waitcnt lgkmcnt(0)
	v_bfe_u32 v79, v98, 16, 1
	v_lshrrev_b32_e32 v67, 16, v67
	v_add3_u32 v79, v98, v79, s43
	v_and_or_b32 v83, v79, s44, v67
	v_add_u32_e32 v67, s22, v70
	s_cmp_eq_u32 s38, 0
	v_lshlrev_b32_e32 v79, 1, v67
	v_and_b32_e32 v84, 0x7f, v67
	v_and_or_b32 v79, v79, s45, v84
	s_cselect_b64 vcc, -1, 0
	v_cndmask_b32_e32 v67, v79, v67, vcc
	v_add_u32_e32 v67, s40, v67
	v_mad_u64_u32 v[100:101], s[2:3], v67, s39, 0
	v_ashrrev_i32_e32 v79, 31, v67
	v_mov_b32_e32 v84, v101
	v_mad_u64_u32 v[102:103], s[2:3], v79, s39, v[84:85]
	v_mov_b32_e32 v101, v102
	s_ashr_i32 s21, s20, 31
	v_lshl_add_u64 v[100:101], v[100:101], 1, s[14:15]
	s_lshl_b64 s[2:3], s[20:21], 1
	v_bfe_u32 v67, v85, 16, 1
	v_lshl_add_u64 v[100:101], v[100:101], 0, s[2:3]
	v_add3_u32 v67, v85, v67, s43
	v_bfe_u32 v79, v87, 16, 1
	v_lshl_add_u64 v[100:101], v[100:101], 0, v[68:69]
	v_lshrrev_b32_e32 v67, 16, v67
	v_add3_u32 v79, v87, v79, s43
	global_store_dwordx4 v[100:101], v[80:83], off nt
	s_nop 1
	v_and_or_b32 v80, v79, s44, v67
	v_bfe_u32 v67, v89, 16, 1
	v_add3_u32 v67, v89, v67, s43
	v_bfe_u32 v79, v91, 16, 1
	v_lshrrev_b32_e32 v67, 16, v67
	v_add3_u32 v79, v91, v79, s43
	v_and_or_b32 v81, v79, s44, v67
	v_bfe_u32 v67, v93, 16, 1
	v_add3_u32 v67, v93, v67, s43
	v_bfe_u32 v79, v95, 16, 1
	v_lshrrev_b32_e32 v67, 16, v67
	v_add3_u32 v79, v95, v79, s43
	v_and_or_b32 v82, v79, s44, v67
	v_bfe_u32 v67, v97, 16, 1
	v_add3_u32 v67, v97, v67, s43
	v_bfe_u32 v79, v99, 16, 1
	v_lshrrev_b32_e32 v67, 16, v67
	v_add3_u32 v79, v99, v79, s43
	v_and_or_b32 v83, v79, s44, v67
	v_add_u32_e32 v67, s22, v1
	v_lshlrev_b32_e32 v79, 1, v67
	v_and_b32_e32 v84, 0x7f, v67
	v_and_or_b32 v79, v79, s45, v84
	v_cndmask_b32_e32 v67, v79, v67, vcc
	v_add_u32_e32 v67, s40, v67
	v_mad_u64_u32 v[84:85], s[16:17], v67, s39, 0
	v_ashrrev_i32_e32 v79, 31, v67
	v_mov_b32_e32 v86, v85
	v_mad_u64_u32 v[86:87], s[16:17], v79, s39, v[86:87]
	v_mov_b32_e32 v85, v86
	v_lshl_add_u64 v[84:85], v[84:85], 1, s[14:15]
	v_lshl_add_u64 v[84:85], v[84:85], 0, s[2:3]
	ds_read2_b32 v[86:87], v73 offset0:16 offset1:24
	v_lshl_add_u64 v[84:85], v[84:85], 0, v[68:69]
	global_store_dwordx4 v[84:85], v[80:83], off nt
	ds_read2_b32 v[84:85], v73 offset0:49 offset1:57
	ds_read2_b32 v[88:89], v73 offset0:82 offset1:90
	ds_read2_b32 v[90:91], v73 offset0:115 offset1:123
	s_waitcnt lgkmcnt(3)
; #define LAS __attribute__((address_space(3)))
; __device__ __forceinline__ unsigned pk2(float lo, float hi) { return f2bf(lo) | (f2bf(hi) << 16); }
;     __device__ __forceinline__ const float* x() const { return (const float*)ld(0); }
;     __device__ __forceinline__ const float* c() const { return (const float*)ld(1); }
; template <bool NT = true> __device__ __forceinline__ void cvt_store(const CvtItem& d, const f32x4 (&v)[8], LAS float* scr, int lane) {
;     const int rr = lane >> 3, c4 = (lane & 7) * 4;
; #pragma unroll
;     for (int q = 0; q < 8; ++q) { LAS float* t = scr + (8 * q + rr) * 33 + c4; t[0] = v[q].x; t[1] = v[q].y; t[2] = v[q].z; t[3] = v[q].w; }
;     asm volatile("s_waitcnt lgkmcnt(0)" ::: "memory");
;     const int c = lane & 7;
; #pragma unroll
;     for (int j = 0; j < 4; ++j) { const int n = (lane >> 3) + 8 * j; const LAS float* s = scr + (8 * c) * 33 + n;
;         u32x4 o; o.x = pk2(s[0 * 33], s[1 * 33]); o.y = pk2(s[2 * 33], s[3 * 33]); o.z = pk2(s[4 * 33], s[5 * 33]); o.w = pk2(s[6 * 33], s[7 * 33]);
;         const int ng = d.n0 + n, drow = d.row_off + (d.ilv ? ((ng >> 7) * 256 + (ng & 127)) : ng);
;         if (NT) __builtin_nontemporal_store(o, (u32x4*)(d.dst + (size_t)drow * d.K + d.k0 + 8 * c)); else *(u32x4*)(d.dst + (size_t)drow * d.K + d.k0 + 8 * c) = o; }
;     asm volatile("s_waitcnt lgkmcnt(0)" ::: "memory");
; __device__ __forceinline__ void convert_moe_items(const Ctx& a, int layer, LAS unsigned char* lds, int it0, int it1, int widx, int nw, int wave, int lane) {
;     ...
;         hb = (it + nw < it1);
;         if (hb) { db = decode(it + nw); cvt_load(db, vb, lane); }
	v_bfe_u32 v67, v86, 16, 1
	v_add3_u32 v67, v86, v67, s43
	s_waitcnt lgkmcnt(2)
	v_bfe_u32 v79, v84, 16, 1
	ds_read2_b32 v[92:93], v73 offset0:148 offset1:156
	v_lshrrev_b32_e32 v67, 16, v67
	v_add3_u32 v79, v84, v79, s43
	ds_read2_b32 v[94:95], v73 offset0:181 offset1:189
	v_and_or_b32 v80, v79, s44, v67
	s_waitcnt lgkmcnt(3)
	v_bfe_u32 v67, v88, 16, 1
	v_add3_u32 v67, v88, v67, s43
	s_waitcnt lgkmcnt(2)
	v_bfe_u32 v79, v90, 16, 1
	ds_read2_b32 v[96:97], v73 offset0:214 offset1:222
	v_lshrrev_b32_e32 v67, 16, v67
	v_add3_u32 v79, v90, v79, s43
	ds_read2_b32 v[98:99], v73 offset0:247 offset1:255
	v_and_or_b32 v81, v79, s44, v67
	s_waitcnt lgkmcnt(3)
	v_bfe_u32 v67, v92, 16, 1
	v_add3_u32 v67, v92, v67, s43
	s_waitcnt lgkmcnt(2)
	v_bfe_u32 v79, v94, 16, 1
	v_lshrrev_b32_e32 v67, 16, v67
	v_add3_u32 v79, v94, v79, s43
	v_and_or_b32 v82, v79, s44, v67
	s_waitcnt lgkmcnt(1)
	v_bfe_u32 v67, v96, 16, 1
	v_add3_u32 v67, v96, v67, s43
	s_waitcnt lgkmcnt(0)
	v_bfe_u32 v79, v98, 16, 1
	v_lshrrev_b32_e32 v67, 16, v67
	v_add3_u32 v79, v98, v79, s43
	v_and_or_b32 v83, v79, s44, v67
	v_add_u32_e32 v67, s22, v71
	v_lshlrev_b32_e32 v79, 1, v67
	v_and_b32_e32 v84, 0x7f, v67
	v_and_or_b32 v79, v79, s45, v84
	v_cndmask_b32_e32 v67, v79, v67, vcc
	v_add_u32_e32 v67, s40, v67
	v_mad_u64_u32 v[100:101], s[16:17], v67, s39, 0
	v_ashrrev_i32_e32 v79, 31, v67
	v_mov_b32_e32 v84, v101
	v_mad_u64_u32 v[102:103], s[16:17], v79, s39, v[84:85]
	v_mov_b32_e32 v101, v102
	v_lshl_add_u64 v[100:101], v[100:101], 1, s[14:15]
	v_bfe_u32 v67, v87, 16, 1
	v_lshl_add_u64 v[100:101], v[100:101], 0, s[2:3]
	v_add3_u32 v67, v87, v67, s43
	v_bfe_u32 v79, v85, 16, 1
	v_lshl_add_u64 v[100:101], v[100:101], 0, v[68:69]
	v_lshrrev_b32_e32 v67, 16, v67
	v_add3_u32 v79, v85, v79, s43
	global_store_dwordx4 v[100:101], v[80:83], off nt
	s_nop 1
	v_and_or_b32 v80, v79, s44, v67
	v_bfe_u32 v67, v89, 16, 1
	v_add3_u32 v67, v89, v67, s43
	v_bfe_u32 v79, v91, 16, 1
	v_lshrrev_b32_e32 v67, 16, v67
	v_add3_u32 v79, v91, v79, s43
	v_and_or_b32 v81, v79, s44, v67
	v_bfe_u32 v67, v93, 16, 1
	v_add3_u32 v67, v93, v67, s43
	v_bfe_u32 v79, v95, 16, 1
	v_lshrrev_b32_e32 v67, 16, v67
	v_add3_u32 v79, v95, v79, s43
	v_and_or_b32 v82, v79, s44, v67
	v_bfe_u32 v67, v97, 16, 1
	v_add3_u32 v67, v97, v67, s43
	v_bfe_u32 v79, v99, 16, 1
	v_lshrrev_b32_e32 v67, 16, v67
	v_add3_u32 v79, v99, v79, s43
	v_and_or_b32 v83, v79, s44, v67
	v_add_u32_e32 v67, s22, v72
	v_lshlrev_b32_e32 v79, 1, v67
	v_and_b32_e32 v84, 0x7f, v67
	v_and_or_b32 v79, v79, s45, v84
	v_cndmask_b32_e32 v67, v79, v67, vcc
	v_add_u32_e32 v67, s40, v67
	v_mad_u64_u32 v[84:85], s[16:17], v67, s39, 0
	v_ashrrev_i32_e32 v79, 31, v67
	v_mov_b32_e32 v86, v85
	v_mad_u64_u32 v[86:87], s[16:17], v79, s39, v[86:87]
	v_mov_b32_e32 v85, v86
	v_lshl_add_u64 v[84:85], v[84:85], 1, s[14:15]
	v_lshl_add_u64 v[84:85], v[84:85], 0, s[2:3]
	v_lshl_add_u64 v[84:85], v[84:85], 0, v[68:69]
	global_store_dwordx4 v[84:85], v[80:83], off nt
	s_add_i32 s2, s42, s37
	s_waitcnt lgkmcnt(0)
	s_cmp_lt_i32 s2, 0x9800
	s_cselect_b64 s[16:17], -1, 0
	s_cmp_gt_i32 s2, 0x97ff
	s_cbranch_scc1 .LBB0_769
	s_mul_hi_i32 s3, s2, 0x2aaaaaab
	s_lshr_b32 s11, s3, 31
	s_ashr_i32 s3, s3, 9
	s_add_i32 s14, s3, s11
	s_mul_i32 s3, s14, 0xc00
	s_ashr_i32 s15, s14, 31
	s_sub_i32 s13, s2, s3
	s_lshl_b64 s[2:3], s[14:15], 21
	s_add_u32 s20, s2, 0x2000000
	s_addc_u32 s21, s3, 0
	s_lshl_b32 s26, s14, 11
	s_cmpk_gt_i32 s13, 0x3ff
	s_mov_b64 s[22:23], -1
	s_cbranch_scc0 .LBB0_787
	s_cmpk_gt_u32 s13, 0x7ff
	s_mov_b64 s[14:15], -1
	s_cbranch_scc0 .LBB0_785
	s_add_i32 s11, s13, 0xfffff800
	s_lshl_b64 s[2:3], s[20:21], 2
	s_add_u32 s2, s34, s2
	s_addc_u32 s3, s33, s3
	s_mov_b64 s[14:15], 0

;     __device__ __forceinline__ const float* x() const { return (const float*)ld(0); }
; __device__ __forceinline__ void convert_moe_items(const Ctx& a, int layer, LAS unsigned char* lds, int it0, int it1, int widx, int nw, int wave, int lane) {
;     ...
;     int it = it0 + widx;
;     if (it >= it1) return;
;     f32x4 va[8], vb[8]; CvtItem da = decode(it), db = da; bool hb = (it + nw < it1);
; PHASE_FN ph_topk(int layer, unsigned* dep, const XcdBarrier& bar) { PH_PRO;
;     ...
;     if ((int)blockIdx.x >= NE || G <= NE) { const int widx = (G <= NE) ? gw : ((int)blockIdx.x - NE) * NWAVES + wave, nw = (G <= NE) ? NGW : (G - NE) * NWAVES;
;         if (layer == 0) convert_moe_items(a, 0, lds, L0_A, L0_B, widx, nw, wave, lane); else convert_moe_items(a, 1, lds, L1_A, MOE_ITEMS, widx, nw, wave, lane); } }
.LBB0_1111:
	v_readlane_b32 s0, v248, 6
	s_cmp_gt_i32 s0, 15
	v_readlane_b32 s1, v248, 7
	s_cselect_b64 s[2:3], -1, 0
	s_waitcnt lgkmcnt(0)
	s_cmp_lt_i32 s96, 17
	s_cselect_b64 s[0:1], -1, 0
	s_or_b64 s[2:3], s[2:3], s[0:1]
	s_and_b64 vcc, exec, s[2:3]
	s_cbranch_vccz .LBB0_1158
	v_readlane_b32 s2, v248, 8
	s_lshr_b32 s22, s2, 6
	v_readlane_b32 s2, v248, 6
	s_lshl_b32 s4, s2, 3
	v_readlane_b32 s3, v248, 7
	s_add_i32 s5, s4, 0xffffff80
	s_and_b64 s[2:3], s[0:1], exec
	s_cselect_b32 s2, s4, s5
	s_add_i32 s3, 0, 0x23f10
	v_mov_b32_e32 v1, s3
	s_add_i32 s3, 0, 0x23ee8
	s_waitcnt vmcnt(0)
	v_mov_b32_e32 v2, s3
	s_add_i32 s3, 0, 0x23ef8
	ds_read_b64 v[6:7], v1
	ds_read2_b64 v[2:5], v2 offset1:1
	v_mov_b32_e32 v1, s3
	ds_read_b64 v[8:9], v1
	s_add_i32 s2, s2, s22
	s_waitcnt lgkmcnt(2)
	v_readfirstlane_b32 s3, v7
	v_readfirstlane_b32 s6, v6
	s_waitcnt lgkmcnt(1)
	v_readfirstlane_b32 s26, v3
	v_readfirstlane_b32 s27, v2
	v_readfirstlane_b32 s28, v5
	v_readfirstlane_b32 s29, v4
	s_waitcnt lgkmcnt(0)
	v_readfirstlane_b32 s30, v9
	s_cmpk_gt_i32 s2, 0x2fff
	v_readfirstlane_b32 s31, v8
	s_cbranch_scc1 .LBB0_1158
	s_add_u32 s4, s6, 0x2530000
	s_addc_u32 s5, s3, 0
	s_add_u32 s6, s6, 0x12530000
	s_addc_u32 s7, s3, 0
	s_add_i32 s35, s2, 0x3000
	s_mul_hi_i32 s2, s35, 0x2aaaaaab
	s_lshr_b32 s3, s2, 31
	s_ashr_i32 s2, s2, 9
	s_add_i32 s2, s2, s3
	s_mul_i32 s3, s2, 0xc00
	s_sub_i32 s15, s35, s3
	s_ashr_i32 s3, s2, 31
	s_lshl_b64 s[10:11], s[2:3], 21
	s_lshl_b32 s17, s2, 11
	s_cmpk_gt_i32 s15, 0x3ff
	s_cbranch_scc0 .LBB0_1117
	s_cmpk_gt_u32 s15, 0x7ff
	s_cbranch_scc0 .LBB0_1123
	s_add_i32 s14, s15, 0xfffff800
	s_lshl_b64 s[2:3], s[10:11], 2
	s_add_u32 s2, s31, s2
	s_addc_u32 s3, s30, s3
	s_mov_b32 s25, 1
	s_cbranch_execz .LBB0_1124
	s_movk_i32 s16, 0x800
	s_movk_i32 s33, 0x400
	s_mov_b32 s25, 0
	s_mov_b32 s34, s17
	s_mov_b64 s[8:9], s[6:7]
	s_cbranch_execz .LBB0_1118
	s_branch .LBB0_1119

; __device__ __forceinline__ void cvt_load(const CvtItem& d, f32x4 (&v)[8], int lane) {
;     const float* p = d.src + (size_t)(d.k0 + (lane >> 3)) * d.N + d.n0 + (lane & 7) * 4;
; #pragma unroll
;     for (int q = 0; q < 8; ++q) v[q] = __builtin_nontemporal_load((const f32x4*)(p + (size_t)(8 * q) * d.N));
; }
; __device__ __forceinline__ void convert_moe_items(const Ctx& a, int layer, LAS unsigned char* lds, int it0, int it1, int widx, int nw, int wave, int lane) {
;     ...
;     f32x4 va[8], vb[8]; CvtItem da = decode(it), db = da; bool hb = (it + nw < it1);
;     cvt_load(da, va, lane);
;     if (hb) { db = decode(it + nw); cvt_load(db, vb, lane); }
.LBB0_1119:
	s_lshl_b32 s10, s96, 3
	s_add_i32 s11, s10, 0xffffff80
	s_and_b64 s[0:1], s[0:1], exec
	s_cselect_b32 s11, s10, s11
	s_lshr_b32 s12, s16, 5
	v_cvt_f32_i32_e32 v1, s12
	s_sext_i32_i16 s0, s14
	v_cvt_f32_i32_e32 v2, s0
	s_ashr_i32 s0, s0, 30
	v_rcp_iflag_f32_e32 v3, v1
	s_or_b32 s10, s0, 1
	v_lshlrev_b32_e32 v4, 2, v0
	v_and_b32_e32 v4, 28, v4
	v_mul_f32_e32 v3, v2, v3
	v_trunc_f32_e32 v3, v3
	v_fma_f32 v2, -v3, v1, v2
	v_cvt_i32_f32_e32 v3, v3
	v_cmp_ge_f32_e64 s[0:1], |v2|, v1
	s_and_b64 s[0:1], s[0:1], exec
	s_cselect_b32 s0, s10, 0
	v_readfirstlane_b32 s1, v3
	s_add_i32 s0, s1, s0
	s_sext_i32_i16 s1, s0
	s_mul_i32 s0, s0, s12
	s_sub_i32 s0, s14, s0
	s_lshl_b32 s10, s1, 6
	s_sext_i32_i16 s0, s0
	v_lshrrev_b32_e32 v1, 3, v214
	s_lshl_b32 s12, s0, 5
	s_add_i32 s19, s35, s11
	v_or_b32_e32 v2, s10, v1
	s_cmpk_lt_i32 s19, 0x6000
	v_mul_hi_i32_i24_e32 v3, s16, v2
	v_mul_i32_i24_e32 v2, s16, v2
	s_cselect_b64 s[14:15], -1, 0
	s_ashr_i32 s13, s12, 31
	v_lshl_add_u64 v[2:3], v[2:3], 2, s[2:3]
	s_mov_b32 s17, 0
	v_lshl_add_u64 v[2:3], s[12:13], 2, v[2:3]
	v_mov_b32_e32 v67, 0
	v_lshlrev_b32_e32 v66, 2, v4
	s_lshl_b64 s[0:1], s[16:17], 5
	v_lshl_add_u64 v[10:11], v[2:3], 0, v[66:67]
	v_lshl_add_u64 v[12:13], v[10:11], 0, s[0:1]
	v_lshl_add_u64 v[18:19], v[12:13], 0, s[0:1]
	v_lshl_add_u64 v[20:21], v[18:19], 0, s[0:1]
	v_lshl_add_u64 v[26:27], v[20:21], 0, s[0:1]
	v_lshl_add_u64 v[28:29], v[26:27], 0, s[0:1]
	v_lshl_add_u64 v[34:35], v[28:29], 0, s[0:1]
	global_load_dwordx4 v[2:5], v[10:11], off nt
	global_load_dwordx4 v[6:9], v[12:13], off nt
	s_nop 0
	global_load_dwordx4 v[10:13], v[18:19], off nt
	global_load_dwordx4 v[14:17], v[20:21], off nt
	s_nop 0
	global_load_dwordx4 v[18:21], v[26:27], off nt
	global_load_dwordx4 v[22:25], v[28:29], off nt
	v_lshl_add_u64 v[36:37], v[34:35], 0, s[0:1]
	global_load_dwordx4 v[26:29], v[34:35], off nt
	global_load_dwordx4 v[30:33], v[36:37], off nt
	s_cmpk_gt_i32 s19, 0x5fff
	s_mov_b64 s[0:1], s[8:9]
	s_mov_b32 s37, s33
	s_mov_b32 s38, s34
	s_mov_b32 s36, s25
	s_mov_b32 s18, s10
	s_mov_b32 s20, s12
	s_cbranch_scc1 .LBB0_1134
	s_mul_hi_i32 s0, s19, 0x2aaaaaab
	s_lshr_b32 s1, s0, 31
	s_ashr_i32 s0, s0, 9
	s_add_i32 s0, s0, s1
	s_mul_i32 s1, s0, 0xc00
	s_sub_i32 s17, s19, s1
	s_ashr_i32 s1, s0, 31
	s_lshl_b64 s[18:19], s[0:1], 21
	s_lshl_b32 s23, s0, 11
	s_cmpk_gt_i32 s17, 0x3ff
	s_cbranch_scc0 .LBB0_1125
	s_cmpk_gt_u32 s17, 0x7ff
	s_cbranch_scc0 .LBB0_1126
	s_add_i32 s13, s17, 0xfffff800
	s_lshl_b64 s[0:1], s[18:19], 2
	s_add_u32 s2, s31, s0
	s_addc_u32 s3, s30, s1
	s_mov_b64 s[0:1], 0
	s_branch .LBB0_1127

; #define LAS __attribute__((address_space(3)))
; __device__ __forceinline__ unsigned pk2(float lo, float hi) { return f2bf(lo) | (f2bf(hi) << 16); }
;     __device__ __forceinline__ const float* x() const { return (const float*)ld(0); }
;     __device__ __forceinline__ const float* c() const { return (const float*)ld(1); }
; template <bool NT = true> __device__ __forceinline__ void cvt_store(const CvtItem& d, const f32x4 (&v)[8], LAS float* scr, int lane) {
;     const int rr = lane >> 3, c4 = (lane & 7) * 4;
; #pragma unroll
;     for (int q = 0; q < 8; ++q) { LAS float* t = scr + (8 * q + rr) * 33 + c4; t[0] = v[q].x; t[1] = v[q].y; t[2] = v[q].z; t[3] = v[q].w; }
;     asm volatile("s_waitcnt lgkmcnt(0)" ::: "memory");
;     const int c = lane & 7;
; #pragma unroll
;     for (int j = 0; j < 4; ++j) { const int n = (lane >> 3) + 8 * j; const LAS float* s = scr + (8 * c) * 33 + n;
;         u32x4 o; o.x = pk2(s[0 * 33], s[1 * 33]); o.y = pk2(s[2 * 33], s[3 * 33]); o.z = pk2(s[4 * 33], s[5 * 33]); o.w = pk2(s[6 * 33], s[7 * 33]);
;         const int ng = d.n0 + n, drow = d.row_off + (d.ilv ? ((ng >> 7) * 256 + (ng & 127)) : ng);
;         if (NT) __builtin_nontemporal_store(o, (u32x4*)(d.dst + (size_t)drow * d.K + d.k0 + 8 * c)); else *(u32x4*)(d.dst + (size_t)drow * d.K + d.k0 + 8 * c) = o; }
;     asm volatile("s_waitcnt lgkmcnt(0)" ::: "memory");
; __device__ __forceinline__ void convert_moe_items(const Ctx& a, int layer, LAS unsigned char* lds, int it0, int it1, int widx, int nw, int wave, int lane) {
;     ...
;     for (;;) {
;         cvt_store(da, va, scr, lane);
;         it += 2 * nw; const bool ha = (it < it1);
;         if (ha) { da = decode(it); cvt_load(da, va, lane); }
;         if (!hb) break;
.Lcvt_p6_t:
	v_add_u32_e32 v79, 0x420, v74
	v_add_u32_e32 v80, 0x428, v74
	v_add_u32_e32 v81, 0x840, v74
	v_add_u32_e32 v82, 0x848, v74
	v_add_u32_e32 v83, 0xc60, v74
	v_add_u32_e32 v84, 0xc68, v74
	v_add_u32_e32 v85, 0x1080, v74
	v_add_u32_e32 v86, 0x1088, v74
	v_add_u32_e32 v87, 0x14a0, v74
	v_add_u32_e32 v88, 0x14a8, v74
	v_add_u32_e32 v89, 0x18c0, v74
	v_add_u32_e32 v90, 0x18c8, v74
	v_add_u32_e32 v91, 0x1ce0, v74
	v_add_u32_e32 v92, 0x1ce8, v74
	s_waitcnt vmcnt(15)
	ds_write2_b32 v74, v2, v3 offset1:1
	ds_write2_b32 v74, v4, v5 offset0:2 offset1:3
	s_waitcnt vmcnt(14)
	ds_write2_b32 v79, v6, v7 offset1:1
	ds_write2_b32 v80, v8, v9 offset1:1
	s_waitcnt vmcnt(13)
	ds_write2_b32 v81, v10, v11 offset1:1
	ds_write2_b32 v82, v12, v13 offset1:1
	s_waitcnt vmcnt(12)
	ds_write2_b32 v83, v14, v15 offset1:1
	ds_write2_b32 v84, v16, v17 offset1:1
	s_waitcnt vmcnt(11)
	ds_write2_b32 v85, v18, v19 offset1:1
	ds_write2_b32 v86, v20, v21 offset1:1
	s_waitcnt vmcnt(10)
	ds_write2_b32 v87, v22, v23 offset1:1
	ds_write2_b32 v88, v24, v25 offset1:1
	s_waitcnt vmcnt(9)
	ds_write2_b32 v89, v26, v27 offset1:1
	ds_write2_b32 v90, v28, v29 offset1:1
	s_waitcnt vmcnt(8)
	ds_write2_b32 v91, v30, v31 offset1:1
	ds_write2_b32 v92, v32, v33 offset1:1
	s_waitcnt lgkmcnt(0)
	ds_read2_b32 v[98:99], v73 offset1:8
	ds_read2_b32 v[100:101], v73 offset0:33 offset1:41
	ds_read2_b32 v[102:103], v73 offset0:66 offset1:74
	ds_read2_b32 v[104:105], v73 offset0:99 offset1:107
	ds_read2_b32 v[106:107], v73 offset0:132 offset1:140
	s_waitcnt lgkmcnt(4)
	v_bfe_u32 v67, v98, 16, 1
	v_add3_u32 v67, v98, v67, s41
	s_waitcnt lgkmcnt(3)
	v_bfe_u32 v93, v100, 16, 1
	v_lshrrev_b32_e32 v67, 16, v67
	v_add3_u32 v93, v100, v93, s41
	ds_read2_b32 v[108:109], v73 offset0:165 offset1:173
	v_and_or_b32 v94, v93, s42, v67
	s_waitcnt lgkmcnt(3)
	v_bfe_u32 v67, v102, 16, 1
	v_add3_u32 v67, v102, v67, s41
	s_waitcnt lgkmcnt(2)
	v_bfe_u32 v93, v104, 16, 1
	ds_read2_b32 v[110:111], v73 offset0:198 offset1:206
	v_lshrrev_b32_e32 v67, 16, v67
	v_add3_u32 v93, v104, v93, s41
	ds_read2_b32 v[112:113], v73 offset0:231 offset1:239
	v_and_or_b32 v95, v93, s42, v67
	s_waitcnt lgkmcnt(3)
	v_bfe_u32 v67, v106, 16, 1
	v_add3_u32 v67, v106, v67, s41
	s_waitcnt lgkmcnt(2)
	v_bfe_u32 v93, v108, 16, 1
	v_lshrrev_b32_e32 v67, 16, v67
	v_add3_u32 v93, v108, v93, s41
	v_and_or_b32 v96, v93, s42, v67
	s_waitcnt lgkmcnt(1)
	v_bfe_u32 v67, v110, 16, 1
	v_add3_u32 v67, v110, v67, s41
	s_waitcnt lgkmcnt(0)
	v_bfe_u32 v93, v112, 16, 1
	s_cmp_eq_u32 s25, 0
	v_lshrrev_b32_e32 v67, 16, v67
	v_add3_u32 v93, v112, v93, s41
	s_cselect_b64 vcc, -1, 0
	s_lshl_b32 s2, s12, 1
	v_and_or_b32 v97, v93, s42, v67
	s_and_b32 s13, s2, 0xffffff00
	v_bitop3_b32 v93, s12, v75, v1 bitop3:0xc8
	v_or_b32_e32 v67, s12, v1
	v_or_b32_e32 v93, s13, v93
	v_cndmask_b32_e32 v67, v93, v67, vcc
	v_add_u32_e32 v67, s34, v67
	v_mad_u64_u32 v[114:115], s[2:3], v67, s33, 0
	v_ashrrev_i32_e32 v93, 31, v67
	v_mov_b32_e32 v98, v115
	v_mad_u64_u32 v[116:117], s[2:3], v93, s33, v[98:99]
	v_mov_b32_e32 v115, v116
	s_ashr_i32 s11, s10, 31
	v_lshl_add_u64 v[114:115], v[114:115], 1, s[8:9]
	s_lshl_b64 s[2:3], s[10:11], 1
	v_bfe_u32 v67, v99, 16, 1
	v_lshl_add_u64 v[114:115], v[114:115], 0, s[2:3]
	v_add3_u32 v67, v99, v67, s41
	v_bfe_u32 v93, v101, 16, 1
	v_lshl_add_u64 v[114:115], v[114:115], 0, v[68:69]
	v_lshrrev_b32_e32 v67, 16, v67
	v_add3_u32 v93, v101, v93, s41
	global_store_dwordx4 v[114:115], v[94:97], off nt
	s_add_i32 s44, s35, s39
	s_cmpk_gt_i32 s44, 0x5fff
	v_and_or_b32 v94, v93, s42, v67
	v_bfe_u32 v67, v103, 16, 1
	v_add3_u32 v67, v103, v67, s41
	v_bfe_u32 v93, v105, 16, 1
	v_lshrrev_b32_e32 v67, 16, v67
	v_add3_u32 v93, v105, v93, s41
	v_and_or_b32 v95, v93, s42, v67
	v_bfe_u32 v67, v107, 16, 1
	v_add3_u32 v67, v107, v67, s41
	v_bfe_u32 v93, v109, 16, 1
	v_lshrrev_b32_e32 v67, 16, v67
	v_add3_u32 v93, v109, v93, s41
	v_and_or_b32 v96, v93, s42, v67
	v_bfe_u32 v67, v111, 16, 1
	v_add3_u32 v67, v111, v67, s41
	v_bfe_u32 v93, v113, 16, 1
	v_lshrrev_b32_e32 v67, 16, v67
	v_add3_u32 v93, v113, v93, s41
	v_and_or_b32 v97, v93, s42, v67
	v_bitop3_b32 v93, s12, v76, v70 bitop3:0xc8
	v_or_b32_e32 v67, s12, v70
	v_or_b32_e32 v93, s13, v93
	v_cndmask_b32_e32 v67, v93, v67, vcc
	v_add_u32_e32 v67, s34, v67
	v_mad_u64_u32 v[98:99], s[22:23], v67, s33, 0
	v_ashrrev_i32_e32 v93, 31, v67
	v_mov_b32_e32 v100, v99
	v_mad_u64_u32 v[100:101], s[22:23], v93, s33, v[100:101]
	v_mov_b32_e32 v99, v100
	v_lshl_add_u64 v[98:99], v[98:99], 1, s[8:9]
	v_lshl_add_u64 v[98:99], v[98:99], 0, s[2:3]
	ds_read2_b32 v[100:101], v73 offset0:16 offset1:24
	v_lshl_add_u64 v[98:99], v[98:99], 0, v[68:69]
	global_store_dwordx4 v[98:99], v[94:97], off nt
	ds_read2_b32 v[98:99], v73 offset0:49 offset1:57
	ds_read2_b32 v[102:103], v73 offset0:82 offset1:90
	ds_read2_b32 v[104:105], v73 offset0:115 offset1:123
	s_waitcnt lgkmcnt(3)
; #define LAS __attribute__((address_space(3)))
; __device__ __forceinline__ unsigned pk2(float lo, float hi) { return f2bf(lo) | (f2bf(hi) << 16); }
;     __device__ __forceinline__ const float* x() const { return (const float*)ld(0); }
;     __device__ __forceinline__ const float* c() const { return (const float*)ld(1); }
; template <bool NT = true> __device__ __forceinline__ void cvt_store(const CvtItem& d, const f32x4 (&v)[8], LAS float* scr, int lane) {
;     const int rr = lane >> 3, c4 = (lane & 7) * 4;
; #pragma unroll
;     for (int q = 0; q < 8; ++q) { LAS float* t = scr + (8 * q + rr) * 33 + c4; t[0] = v[q].x; t[1] = v[q].y; t[2] = v[q].z; t[3] = v[q].w; }
;     asm volatile("s_waitcnt lgkmcnt(0)" ::: "memory");
;     const int c = lane & 7;
; #pragma unroll
;     for (int j = 0; j < 4; ++j) { const int n = (lane >> 3) + 8 * j; const LAS float* s = scr + (8 * c) * 33 + n;
;         u32x4 o; o.x = pk2(s[0 * 33], s[1 * 33]); o.y = pk2(s[2 * 33], s[3 * 33]); o.z = pk2(s[4 * 33], s[5 * 33]); o.w = pk2(s[6 * 33], s[7 * 33]);
;         const int ng = d.n0 + n, drow = d.row_off + (d.ilv ? ((ng >> 7) * 256 + (ng & 127)) : ng);
;         if (NT) __builtin_nontemporal_store(o, (u32x4*)(d.dst + (size_t)drow * d.K + d.k0 + 8 * c)); else *(u32x4*)(d.dst + (size_t)drow * d.K + d.k0 + 8 * c) = o; }
;     asm volatile("s_waitcnt lgkmcnt(0)" ::: "memory");
; __device__ __forceinline__ void convert_moe_items(const Ctx& a, int layer, LAS unsigned char* lds, int it0, int it1, int widx, int nw, int wave, int lane) {
;     ...
;     auto decode = [&](int it) { CvtItem d; const int e = it / PER_E; int r = it % PER_E; const size_t eo = ((size_t)layer * NE + e) * (size_t)DM * FE;
;         if (r < I_G)          { d.src = wg + eo; d.dst = WGU; d.N = FE; d.K = DM; d.row_off = e * 2048; d.ilv = 1; }
;         else if (r < 2 * I_G) { r -= I_G; d.src = wu + eo; d.dst = WGU; d.N = FE; d.K = DM; d.row_off = e * 2048 + 128; d.ilv = 1; }
;         else                  { r -= 2 * I_G; d.src = wd + eo; d.dst = WD; d.N = DM; d.K = FE; d.row_off = e * 2048; d.ilv = 0; }
;         const int nblk = d.N / 32; d.k0 = 64 * (r / nblk); d.n0 = 32 * (r % nblk); return d; };
	v_bfe_u32 v67, v100, 16, 1
	v_add3_u32 v67, v100, v67, s41
	s_waitcnt lgkmcnt(2)
	v_bfe_u32 v93, v98, 16, 1
	ds_read2_b32 v[106:107], v73 offset0:148 offset1:156
	v_lshrrev_b32_e32 v67, 16, v67
	v_add3_u32 v93, v98, v93, s41
	ds_read2_b32 v[108:109], v73 offset0:181 offset1:189
	v_and_or_b32 v94, v93, s42, v67
	s_waitcnt lgkmcnt(3)
	v_bfe_u32 v67, v102, 16, 1
	v_add3_u32 v67, v102, v67, s41
	s_waitcnt lgkmcnt(2)
	v_bfe_u32 v93, v104, 16, 1
	ds_read2_b32 v[110:111], v73 offset0:214 offset1:222
	v_lshrrev_b32_e32 v67, 16, v67
	v_add3_u32 v93, v104, v93, s41
	ds_read2_b32 v[112:113], v73 offset0:247 offset1:255
	v_and_or_b32 v95, v93, s42, v67
	s_waitcnt lgkmcnt(3)
	v_bfe_u32 v67, v106, 16, 1
	v_add3_u32 v67, v106, v67, s41
	s_waitcnt lgkmcnt(2)
	v_bfe_u32 v93, v108, 16, 1
	v_lshrrev_b32_e32 v67, 16, v67
	v_add3_u32 v93, v108, v93, s41
	v_and_or_b32 v96, v93, s42, v67
	s_waitcnt lgkmcnt(1)
	v_bfe_u32 v67, v110, 16, 1
	v_add3_u32 v67, v110, v67, s41
	s_waitcnt lgkmcnt(0)
	v_bfe_u32 v93, v112, 16, 1
	v_lshrrev_b32_e32 v67, 16, v67
	v_add3_u32 v93, v112, v93, s41
	v_and_or_b32 v97, v93, s42, v67
	v_bitop3_b32 v93, s12, v77, v71 bitop3:0xc8
	v_or_b32_e32 v67, s12, v71
	v_or_b32_e32 v93, s13, v93
	v_cndmask_b32_e32 v67, v93, v67, vcc
	v_add_u32_e32 v67, s34, v67
	v_mad_u64_u32 v[114:115], s[22:23], v67, s33, 0
	v_ashrrev_i32_e32 v93, 31, v67
	v_mov_b32_e32 v98, v115
	v_mad_u64_u32 v[116:117], s[22:23], v93, s33, v[98:99]
	v_mov_b32_e32 v115, v116
	v_lshl_add_u64 v[114:115], v[114:115], 1, s[8:9]
	v_bfe_u32 v67, v101, 16, 1
	v_lshl_add_u64 v[114:115], v[114:115], 0, s[2:3]
	v_add3_u32 v67, v101, v67, s41
	v_bfe_u32 v93, v99, 16, 1
	v_lshl_add_u64 v[114:115], v[114:115], 0, v[68:69]
	v_lshrrev_b32_e32 v67, 16, v67
	v_add3_u32 v93, v99, v93, s41
	global_store_dwordx4 v[114:115], v[94:97], off nt
	s_nop 1
	v_and_or_b32 v94, v93, s42, v67
	v_bfe_u32 v67, v103, 16, 1
	v_add3_u32 v67, v103, v67, s41
	v_bfe_u32 v93, v105, 16, 1
	v_lshrrev_b32_e32 v67, 16, v67
	v_add3_u32 v93, v105, v93, s41
	v_and_or_b32 v95, v93, s42, v67
	v_bfe_u32 v67, v107, 16, 1
	v_add3_u32 v67, v107, v67, s41
	v_bfe_u32 v93, v109, 16, 1
	v_lshrrev_b32_e32 v67, 16, v67
	v_add3_u32 v93, v109, v93, s41
	v_and_or_b32 v96, v93, s42, v67
	v_bfe_u32 v67, v111, 16, 1
	v_add3_u32 v67, v111, v67, s41
	v_bfe_u32 v93, v113, 16, 1
	v_lshrrev_b32_e32 v67, 16, v67
	v_add3_u32 v93, v113, v93, s41
	v_and_or_b32 v97, v93, s42, v67
	v_bitop3_b32 v93, s12, v78, v72 bitop3:0xc8
	v_or_b32_e32 v67, s12, v72
	v_or_b32_e32 v93, s13, v93
	v_cndmask_b32_e32 v67, v93, v67, vcc
	v_add_u32_e32 v67, s34, v67
	v_mad_u64_u32 v[98:99], s[22:23], v67, s33, 0
	v_ashrrev_i32_e32 v93, 31, v67
	v_mov_b32_e32 v100, v99
	v_mad_u64_u32 v[100:101], s[22:23], v93, s33, v[100:101]
	v_mov_b32_e32 v99, v100
	v_lshl_add_u64 v[98:99], v[98:99], 1, s[8:9]
	v_lshl_add_u64 v[98:99], v[98:99], 0, s[2:3]
	v_lshl_add_u64 v[98:99], v[98:99], 0, v[68:69]
	global_store_dwordx4 v[98:99], v[94:97], off nt
	s_waitcnt lgkmcnt(0)
	s_cselect_b64 s[22:23], -1, 0
	s_and_b64 vcc, exec, s[22:23]
	s_cbranch_vccnz .LBB0_1147
	s_mul_hi_i32 s2, s44, 0x2aaaaaab
	s_lshr_b32 s3, s2, 31
	s_ashr_i32 s2, s2, 9
	s_add_i32 s24, s2, s3
	s_mul_i32 s2, s24, 0xfffff400
	s_ashr_i32 s25, s24, 31
	s_add_i32 s21, s44, s2
	s_lshl_b64 s[10:11], s[24:25], 21
	s_lshl_b32 s45, s24, 11
	s_cmpk_gt_i32 s21, 0x3ff
	s_mov_b64 s[12:13], -1
	s_cbranch_scc0 .LBB0_1144
	s_mul_i32 s2, s24, 0xc00
	s_sub_i32 s12, s44, s2
	s_cmpk_gt_u32 s21, 0x7ff
	s_mov_b64 s[8:9], -1
	s_cbranch_scc0 .LBB0_1142
	s_add_i32 s19, s12, 0xfffff800
	s_lshl_b64 s[2:3], s[10:11], 2
	s_add_u32 s2, s31, s2
	s_addc_u32 s3, s30, s3
	s_mov_b64 s[8:9], 0

; #define LAS __attribute__((address_space(3)))
; __device__ __forceinline__ unsigned pk2(float lo, float hi) { return f2bf(lo) | (f2bf(hi) << 16); }
;     __device__ __forceinline__ const float* x() const { return (const float*)ld(0); }
;     __device__ __forceinline__ const float* c() const { return (const float*)ld(1); }
; template <bool NT = true> __device__ __forceinline__ void cvt_store(const CvtItem& d, const f32x4 (&v)[8], LAS float* scr, int lane) {
;     const int rr = lane >> 3, c4 = (lane & 7) * 4;
; #pragma unroll
;     for (int q = 0; q < 8; ++q) { LAS float* t = scr + (8 * q + rr) * 33 + c4; t[0] = v[q].x; t[1] = v[q].y; t[2] = v[q].z; t[3] = v[q].w; }
;     asm volatile("s_waitcnt lgkmcnt(0)" ::: "memory");
;     const int c = lane & 7;
; #pragma unroll
;     for (int j = 0; j < 4; ++j) { const int n = (lane >> 3) + 8 * j; const LAS float* s = scr + (8 * c) * 33 + n;
;         u32x4 o; o.x = pk2(s[0 * 33], s[1 * 33]); o.y = pk2(s[2 * 33], s[3 * 33]); o.z = pk2(s[4 * 33], s[5 * 33]); o.w = pk2(s[6 * 33], s[7 * 33]);
;         const int ng = d.n0 + n, drow = d.row_off + (d.ilv ? ((ng >> 7) * 256 + (ng & 127)) : ng);
;         if (NT) __builtin_nontemporal_store(o, (u32x4*)(d.dst + (size_t)drow * d.K + d.k0 + 8 * c)); else *(u32x4*)(d.dst + (size_t)drow * d.K + d.k0 + 8 * c) = o; }
;     asm volatile("s_waitcnt lgkmcnt(0)" ::: "memory");
; __device__ __forceinline__ void convert_moe_items(const Ctx& a, int layer, LAS unsigned char* lds, int it0, int it1, int widx, int nw, int wave, int lane) {
;     ...
;         cvt_store(db, vb, scr, lane);
;         hb = (it + nw < it1);
;         if (hb) { db = decode(it + nw); cvt_load(db, vb, lane); }
.Lcvt_p6_m:
	s_waitcnt vmcnt(12)
	ds_write2_b32 v74, v34, v35 offset1:1
	ds_write2_b32 v74, v36, v37 offset0:2 offset1:3
	ds_write2_b32 v79, v38, v39 offset1:1
	ds_write2_b32 v80, v40, v41 offset1:1
	ds_write2_b32 v81, v42, v43 offset1:1
	ds_write2_b32 v82, v44, v45 offset1:1
	ds_write2_b32 v83, v46, v47 offset1:1
	ds_write2_b32 v84, v48, v49 offset1:1
	ds_write2_b32 v85, v50, v51 offset1:1
	ds_write2_b32 v86, v52, v53 offset1:1
	ds_write2_b32 v87, v54, v55 offset1:1
	ds_write2_b32 v88, v56, v57 offset1:1
	ds_write2_b32 v89, v58, v59 offset1:1
	ds_write2_b32 v90, v60, v61 offset1:1
	ds_write2_b32 v91, v62, v63 offset1:1
	ds_write2_b32 v92, v64, v65 offset1:1
	s_waitcnt lgkmcnt(0)
	ds_read2_b32 v[84:85], v73 offset1:8
	ds_read2_b32 v[86:87], v73 offset0:33 offset1:41
	ds_read2_b32 v[88:89], v73 offset0:66 offset1:74
	ds_read2_b32 v[90:91], v73 offset0:99 offset1:107
	ds_read2_b32 v[92:93], v73 offset0:132 offset1:140
	s_waitcnt lgkmcnt(4)
	v_bfe_u32 v67, v84, 16, 1
	v_add3_u32 v67, v84, v67, s41
	s_waitcnt lgkmcnt(3)
	v_bfe_u32 v79, v86, 16, 1
	v_lshrrev_b32_e32 v67, 16, v67
	v_add3_u32 v79, v86, v79, s41
	ds_read2_b32 v[94:95], v73 offset0:165 offset1:173
	v_and_or_b32 v80, v79, s42, v67
	s_waitcnt lgkmcnt(3)
	v_bfe_u32 v67, v88, 16, 1
	v_add3_u32 v67, v88, v67, s41
	s_waitcnt lgkmcnt(2)
	v_bfe_u32 v79, v90, 16, 1
	ds_read2_b32 v[96:97], v73 offset0:198 offset1:206
	v_lshrrev_b32_e32 v67, 16, v67
	v_add3_u32 v79, v90, v79, s41
	ds_read2_b32 v[98:99], v73 offset0:231 offset1:239
	v_and_or_b32 v81, v79, s42, v67
	s_waitcnt lgkmcnt(3)
	v_bfe_u32 v67, v92, 16, 1
	v_add3_u32 v67, v92, v67, s41
	s_waitcnt lgkmcnt(2)
	v_bfe_u32 v79, v94, 16, 1
	v_lshrrev_b32_e32 v67, 16, v67
	v_add3_u32 v79, v94, v79, s41
	v_and_or_b32 v82, v79, s42, v67
	s_waitcnt lgkmcnt(1)
	v_bfe_u32 v67, v96, 16, 1
	v_add3_u32 v67, v96, v67, s41
	s_waitcnt lgkmcnt(0)
	v_bfe_u32 v79, v98, 16, 1
	v_lshrrev_b32_e32 v67, 16, v67
	v_add3_u32 v79, v98, v79, s41
	v_and_or_b32 v83, v79, s42, v67
	v_add_u32_e32 v67, s20, v1
	s_cmp_eq_u32 s36, 0
	v_lshlrev_b32_e32 v79, 1, v67
	v_and_b32_e32 v84, 0x7f, v67
	v_and_or_b32 v79, v79, s43, v84
	s_cselect_b64 vcc, -1, 0
	v_cndmask_b32_e32 v67, v79, v67, vcc
	v_add_u32_e32 v67, s38, v67
	v_mad_u64_u32 v[100:101], s[2:3], v67, s37, 0
	v_ashrrev_i32_e32 v79, 31, v67
	v_mov_b32_e32 v84, v101
	v_mad_u64_u32 v[102:103], s[2:3], v79, s37, v[84:85]
	v_mov_b32_e32 v101, v102
	s_ashr_i32 s19, s18, 31
	v_lshl_add_u64 v[100:101], v[100:101], 1, s[0:1]
	s_lshl_b64 s[2:3], s[18:19], 1
	v_bfe_u32 v67, v85, 16, 1
	v_lshl_add_u64 v[100:101], v[100:101], 0, s[2:3]
	v_add3_u32 v67, v85, v67, s41
	v_bfe_u32 v79, v87, 16, 1
	v_lshl_add_u64 v[100:101], v[100:101], 0, v[68:69]
	v_lshrrev_b32_e32 v67, 16, v67
	v_add3_u32 v79, v87, v79, s41
	global_store_dwordx4 v[100:101], v[80:83], off nt
	s_nop 1
	v_and_or_b32 v80, v79, s42, v67
	v_bfe_u32 v67, v89, 16, 1
	v_add3_u32 v67, v89, v67, s41
	v_bfe_u32 v79, v91, 16, 1
	v_lshrrev_b32_e32 v67, 16, v67
	v_add3_u32 v79, v91, v79, s41
	v_and_or_b32 v81, v79, s42, v67
	v_bfe_u32 v67, v93, 16, 1
	v_add3_u32 v67, v93, v67, s41
	v_bfe_u32 v79, v95, 16, 1
	v_lshrrev_b32_e32 v67, 16, v67
	v_add3_u32 v79, v95, v79, s41
	v_and_or_b32 v82, v79, s42, v67
	v_bfe_u32 v67, v97, 16, 1
	v_add3_u32 v67, v97, v67, s41
	v_bfe_u32 v79, v99, 16, 1
	v_lshrrev_b32_e32 v67, 16, v67
	v_add3_u32 v79, v99, v79, s41
	v_and_or_b32 v83, v79, s42, v67
	v_add_u32_e32 v67, s20, v70
	v_lshlrev_b32_e32 v79, 1, v67
	v_and_b32_e32 v84, 0x7f, v67
	v_and_or_b32 v79, v79, s43, v84
	v_cndmask_b32_e32 v67, v79, v67, vcc
	v_add_u32_e32 v67, s38, v67
	v_mad_u64_u32 v[84:85], s[14:15], v67, s37, 0
	v_ashrrev_i32_e32 v79, 31, v67
	v_mov_b32_e32 v86, v85
	v_mad_u64_u32 v[86:87], s[14:15], v79, s37, v[86:87]
	v_mov_b32_e32 v85, v86
	v_lshl_add_u64 v[84:85], v[84:85], 1, s[0:1]
	v_lshl_add_u64 v[84:85], v[84:85], 0, s[2:3]
	ds_read2_b32 v[86:87], v73 offset0:16 offset1:24
	v_lshl_add_u64 v[84:85], v[84:85], 0, v[68:69]
	global_store_dwordx4 v[84:85], v[80:83], off nt
	ds_read2_b32 v[84:85], v73 offset0:49 offset1:57
	ds_read2_b32 v[88:89], v73 offset0:82 offset1:90
	ds_read2_b32 v[90:91], v73 offset0:115 offset1:123
	s_waitcnt lgkmcnt(3)
; #define LAS __attribute__((address_space(3)))
; __device__ __forceinline__ unsigned pk2(float lo, float hi) { return f2bf(lo) | (f2bf(hi) << 16); }
;     __device__ __forceinline__ const float* x() const { return (const float*)ld(0); }
;     __device__ __forceinline__ const float* c() const { return (const float*)ld(1); }
; template <bool NT = true> __device__ __forceinline__ void cvt_store(const CvtItem& d, const f32x4 (&v)[8], LAS float* scr, int lane) {
;     const int rr = lane >> 3, c4 = (lane & 7) * 4;
; #pragma unroll
;     for (int q = 0; q < 8; ++q) { LAS float* t = scr + (8 * q + rr) * 33 + c4; t[0] = v[q].x; t[1] = v[q].y; t[2] = v[q].z; t[3] = v[q].w; }
;     asm volatile("s_waitcnt lgkmcnt(0)" ::: "memory");
;     const int c = lane & 7;
; #pragma unroll
;     for (int j = 0; j < 4; ++j) { const int n = (lane >> 3) + 8 * j; const LAS float* s = scr + (8 * c) * 33 + n;
;         u32x4 o; o.x = pk2(s[0 * 33], s[1 * 33]); o.y = pk2(s[2 * 33], s[3 * 33]); o.z = pk2(s[4 * 33], s[5 * 33]); o.w = pk2(s[6 * 33], s[7 * 33]);
;         const int ng = d.n0 + n, drow = d.row_off + (d.ilv ? ((ng >> 7) * 256 + (ng & 127)) : ng);
;         if (NT) __builtin_nontemporal_store(o, (u32x4*)(d.dst + (size_t)drow * d.K + d.k0 + 8 * c)); else *(u32x4*)(d.dst + (size_t)drow * d.K + d.k0 + 8 * c) = o; }
;     asm volatile("s_waitcnt lgkmcnt(0)" ::: "memory");
; __device__ __forceinline__ void convert_moe_items(const Ctx& a, int layer, LAS unsigned char* lds, int it0, int it1, int widx, int nw, int wave, int lane) {
;     ...
;         hb = (it + nw < it1);
;         if (hb) { db = decode(it + nw); cvt_load(db, vb, lane); }
	v_bfe_u32 v67, v86, 16, 1
	v_add3_u32 v67, v86, v67, s41
	s_waitcnt lgkmcnt(2)
	v_bfe_u32 v79, v84, 16, 1
	ds_read2_b32 v[92:93], v73 offset0:148 offset1:156
	v_lshrrev_b32_e32 v67, 16, v67
	v_add3_u32 v79, v84, v79, s41
	ds_read2_b32 v[94:95], v73 offset0:181 offset1:189
	v_and_or_b32 v80, v79, s42, v67
	s_waitcnt lgkmcnt(3)
	v_bfe_u32 v67, v88, 16, 1
	v_add3_u32 v67, v88, v67, s41
	s_waitcnt lgkmcnt(2)
	v_bfe_u32 v79, v90, 16, 1
	ds_read2_b32 v[96:97], v73 offset0:214 offset1:222
	v_lshrrev_b32_e32 v67, 16, v67
	v_add3_u32 v79, v90, v79, s41
	ds_read2_b32 v[98:99], v73 offset0:247 offset1:255
	v_and_or_b32 v81, v79, s42, v67
	s_waitcnt lgkmcnt(3)
	v_bfe_u32 v67, v92, 16, 1
	v_add3_u32 v67, v92, v67, s41
	s_waitcnt lgkmcnt(2)
	v_bfe_u32 v79, v94, 16, 1
	v_lshrrev_b32_e32 v67, 16, v67
	v_add3_u32 v79, v94, v79, s41
	v_and_or_b32 v82, v79, s42, v67
	s_waitcnt lgkmcnt(1)
	v_bfe_u32 v67, v96, 16, 1
	v_add3_u32 v67, v96, v67, s41
	s_waitcnt lgkmcnt(0)
	v_bfe_u32 v79, v98, 16, 1
	v_lshrrev_b32_e32 v67, 16, v67
	v_add3_u32 v79, v98, v79, s41
	v_and_or_b32 v83, v79, s42, v67
	v_add_u32_e32 v67, s20, v71
	v_lshlrev_b32_e32 v79, 1, v67
	v_and_b32_e32 v84, 0x7f, v67
	v_and_or_b32 v79, v79, s43, v84
	v_cndmask_b32_e32 v67, v79, v67, vcc
	v_add_u32_e32 v67, s38, v67
	v_mad_u64_u32 v[100:101], s[14:15], v67, s37, 0
	v_ashrrev_i32_e32 v79, 31, v67
	v_mov_b32_e32 v84, v101
	v_mad_u64_u32 v[102:103], s[14:15], v79, s37, v[84:85]
	v_mov_b32_e32 v101, v102
	v_lshl_add_u64 v[100:101], v[100:101], 1, s[0:1]
	v_bfe_u32 v67, v87, 16, 1
	v_lshl_add_u64 v[100:101], v[100:101], 0, s[2:3]
	v_add3_u32 v67, v87, v67, s41
	v_bfe_u32 v79, v85, 16, 1
	v_lshl_add_u64 v[100:101], v[100:101], 0, v[68:69]
	v_lshrrev_b32_e32 v67, 16, v67
	v_add3_u32 v79, v85, v79, s41
	global_store_dwordx4 v[100:101], v[80:83], off nt
	s_nop 1
	v_and_or_b32 v80, v79, s42, v67
	v_bfe_u32 v67, v89, 16, 1
	v_add3_u32 v67, v89, v67, s41
	v_bfe_u32 v79, v91, 16, 1
	v_lshrrev_b32_e32 v67, 16, v67
	v_add3_u32 v79, v91, v79, s41
	v_and_or_b32 v81, v79, s42, v67
	v_bfe_u32 v67, v93, 16, 1
	v_add3_u32 v67, v93, v67, s41
	v_bfe_u32 v79, v95, 16, 1
	v_lshrrev_b32_e32 v67, 16, v67
	v_add3_u32 v79, v95, v79, s41
	v_and_or_b32 v82, v79, s42, v67
	v_bfe_u32 v67, v97, 16, 1
	v_add3_u32 v67, v97, v67, s41
	v_bfe_u32 v79, v99, 16, 1
	v_lshrrev_b32_e32 v67, 16, v67
	v_add3_u32 v79, v99, v79, s41
	v_and_or_b32 v83, v79, s42, v67
	v_add_u32_e32 v67, s20, v72
	v_lshlrev_b32_e32 v79, 1, v67
	v_and_b32_e32 v84, 0x7f, v67
	v_and_or_b32 v79, v79, s43, v84
	v_cndmask_b32_e32 v67, v79, v67, vcc
	v_add_u32_e32 v67, s38, v67
	v_mad_u64_u32 v[84:85], s[14:15], v67, s37, 0
	v_ashrrev_i32_e32 v79, 31, v67
	v_mov_b32_e32 v86, v85
	v_mad_u64_u32 v[86:87], s[14:15], v79, s37, v[86:87]
	v_mov_b32_e32 v85, v86
	v_lshl_add_u64 v[84:85], v[84:85], 1, s[0:1]
	v_lshl_add_u64 v[84:85], v[84:85], 0, s[2:3]
	v_lshl_add_u64 v[84:85], v[84:85], 0, v[68:69]
	global_store_dwordx4 v[84:85], v[80:83], off nt
	s_add_i32 s2, s40, s35
	s_waitcnt lgkmcnt(0)
	s_cmpk_lt_i32 s2, 0x6000
	s_cselect_b64 s[14:15], -1, 0
	s_cmpk_gt_i32 s2, 0x5fff
	s_cbranch_scc1 .LBB0_1136
	s_mul_hi_i32 s0, s2, 0x2aaaaaab
	s_lshr_b32 s1, s0, 31
	s_ashr_i32 s0, s0, 9
	s_add_i32 s0, s0, s1
	s_mul_i32 s1, s0, 0xc00
	s_sub_i32 s13, s2, s1
	s_ashr_i32 s1, s0, 31
	s_lshl_b64 s[18:19], s[0:1], 21
	s_lshl_b32 s24, s0, 11
	s_cmpk_gt_i32 s13, 0x3ff
	s_mov_b64 s[20:21], -1
	s_cbranch_scc0 .LBB0_1154
	s_cmpk_gt_u32 s13, 0x7ff
	s_mov_b64 s[0:1], -1
	s_cbranch_scc0 .LBB0_1152
	s_add_i32 s11, s13, 0xfffff800
	s_lshl_b64 s[0:1], s[18:19], 2
	s_add_u32 s2, s31, s0
	s_addc_u32 s3, s30, s1
	s_mov_b64 s[0:1], 0

;     __device__ __forceinline__ const float* x() const { return (const float*)ld(0); }
; __device__ __forceinline__ void convert_moe_items(const Ctx& a, int layer, LAS unsigned char* lds, int it0, int it1, int widx, int nw, int wave, int lane) {
;     ...
;     int it = it0 + widx;
;     if (it >= it1) return;
;     f32x4 va[8], vb[8]; CvtItem da = decode(it), db = da; bool hb = (it + nw < it1);
; PHASE_FN ph_topk(int layer, unsigned* dep, const XcdBarrier& bar) { PH_PRO;
;     ...
;     if ((int)blockIdx.x >= NE || G <= NE) { const int widx = (G <= NE) ? gw : ((int)blockIdx.x - NE) * NWAVES + wave, nw = (G <= NE) ? NGW : (G - NE) * NWAVES;
;         if (layer == 0) convert_moe_items(a, 0, lds, L0_A, L0_B, widx, nw, wave, lane); else convert_moe_items(a, 1, lds, L1_A, MOE_ITEMS, widx, nw, wave, lane); } }
.LBB0_1967:
	v_readlane_b32 s0, v248, 6
	v_readlane_b32 s1, v248, 7
	s_cmp_gt_i32 s0, 15
	s_cselect_b64 s[0:1], -1, 0
	s_waitcnt lgkmcnt(0)
	s_cmp_lt_i32 s96, 17
	s_cselect_b64 s[8:9], -1, 0
	s_or_b64 s[0:1], s[0:1], s[8:9]
	s_and_b64 vcc, exec, s[0:1]
	s_cbranch_vccz .LBB0_2014
	v_readlane_b32 s0, v248, 8
	s_lshr_b32 s22, s0, 6
	v_readlane_b32 s0, v248, 6
	s_lshl_b32 s2, s0, 3
	v_readlane_b32 s1, v248, 7
	s_add_i32 s3, s2, 0xffffff80
	s_and_b64 s[0:1], s[8:9], exec
	s_cselect_b32 s2, s2, s3
	s_add_i32 s0, 0, 0x23f10
	v_mov_b32_e32 v1, s0
	s_add_i32 s0, 0, 0x23ee8
	s_waitcnt vmcnt(0)
	v_mov_b32_e32 v2, s0
	s_add_i32 s0, 0, 0x23ef8
	ds_read_b64 v[6:7], v1
	ds_read2_b64 v[2:5], v2 offset1:1
	v_mov_b32_e32 v1, s0
	ds_read_b64 v[8:9], v1
	s_add_i32 s2, s2, s22
	s_waitcnt lgkmcnt(2)
	v_readfirstlane_b32 s3, v7
	v_readfirstlane_b32 s4, v6
	s_waitcnt lgkmcnt(1)
	v_readfirstlane_b32 s26, v3
	v_readfirstlane_b32 s27, v2
	v_readfirstlane_b32 s28, v5
	v_readfirstlane_b32 s29, v4
	s_waitcnt lgkmcnt(0)
	v_readfirstlane_b32 s30, v9
	s_cmpk_gt_i32 s2, 0x27ff
	v_readfirstlane_b32 s31, v8
	s_cbranch_scc1 .LBB0_2014
	s_add_u32 s0, s4, 0xa530000
	s_addc_u32 s1, s3, 0
	s_add_u32 s4, s4, 0x16530000
	s_addc_u32 s5, s3, 0
	s_add_i32 s35, s2, 0x9800
	s_mul_hi_i32 s2, s35, 0x2aaaaaab
	s_lshr_b32 s3, s2, 31
	s_ashr_i32 s2, s2, 9
	s_add_i32 s2, s2, s3
	s_mul_i32 s3, s2, 0xc00
	s_sub_i32 s13, s35, s3
	s_ashr_i32 s3, s2, 31
	s_lshl_b64 s[6:7], s[2:3], 21
	s_add_u32 s10, s6, 0x2000000
	s_addc_u32 s11, s7, 0
	s_lshl_b32 s17, s2, 11
	s_cmpk_gt_i32 s13, 0x3ff
	s_cbranch_scc0 .LBB0_1973
	s_cmpk_gt_u32 s13, 0x7ff
	s_cbranch_scc0 .LBB0_1979
	s_add_i32 s16, s13, 0xfffff800
	s_lshl_b64 s[2:3], s[10:11], 2
	s_add_u32 s2, s31, s2
	s_addc_u32 s3, s30, s3
	s_mov_b32 s25, 1
	s_cbranch_execz .LBB0_1980
	s_movk_i32 s12, 0x800
	s_movk_i32 s33, 0x400
	s_mov_b32 s25, 0
	s_mov_b32 s34, s17
	s_mov_b64 s[6:7], s[4:5]
	s_cbranch_execz .LBB0_1974
	s_branch .LBB0_1975
